# GEMM K-loops: removed mid-block setprio 0/1 flips and the redundant post-barrier lgkmcnt(0) ahead of each MFMA block
# speedup vs baseline: 1.0176x; 1.0044x over previous
; #define PG8_STAGE(bufoff, gbase, voff) do { _Pragma("unroll") for (int _i = 0; _i < 2; ++_i) \
;         __builtin_amdgcn_global_load_lds((const unsigned*)((const char*)(gbase) + (voff)[_i]), (PG8_LAS unsigned*)(lds + (bufoff) + ldsw + _i * 8192), 16, 0, 0); } while (0)
; #define PG8_LDA(dst, b, h) do { _Pragma("unroll") for (int m = 0; m < 4; ++m) _Pragma("unroll") for (int k = 0; k < 2; ++k) dst[m][k] = *(const PG8_LAS bf16x8*)(lds + PG8_SA(b, h) + aoff + m * 2048 + k * 1024); } while (0)
; #define PG8_LDB(dst, b, h) do { _Pragma("unroll") for (int n = 0; n < 2; ++n) _Pragma("unroll") for (int k = 0; k < 2; ++k) dst[n][k] = *(const PG8_LAS bf16x8*)(lds + PG8_SB(b, h) + boff + n * 2048 + k * 1024); } while (0)
; #define PG8_MMA(ai, bj, At, Bt) do { __builtin_amdgcn_s_setprio(1); _Pragma("unroll") for (int m = 0; m < 4; ++m) _Pragma("unroll") for (int n = 0; n < 2; ++n) _Pragma("unroll") for (int k = 0; k < 2; ++k) \
;         acc[ai][bj][m][n] = __builtin_amdgcn_mfma_f32_16x16x32_bf16(Bt[n][k], At[m][k], acc[ai][bj][m][n], 0, 0, 0); __builtin_amdgcn_s_setprio(0); } while (0)
; #define PG8_WAIT_V(n) asm volatile("s_waitcnt vmcnt(" #n ")" ::: "memory")
; template <class Epi, class Sched, bool ALIGN_EPI = false, bool SP2 = false>
; __device__ __forceinline__ void gemm_phase(PG8_LAS unsigned char* lds, const Gemm g, const Sched& S, const Epi& E) {
;     ...
;             PG8_LDB(B0, 0, 0); PG8_LDB(B1, 0, 1); PG8_SCHED; PG8_LDA(At, 0, 0); PG8_STAGEA(PG8_SA(1, 1), a1, 1, false);
;             PG8_WAIT_V(8); PG8_WAIT_L(0); PG8_BAR; PG8_MMA(0, 0, At, B0); PG8_MMA(0, 1, At, B1); PG8_BAR; PG8_SCHED;
;             PG8_LDA(At, 0, 1); PG8_STAGE(PG8_SB(0, 0), b2, voffB); PG8_STAGE(PG8_SB(0, 1), b2 + hstep, voffB); PG8_STAGEA(PG8_SA(0, 0), a2, 0, last);
;             PG8_WAIT_V(8); PG8_WAIT_L(0); PG8_BAR; PG8_MMA(1, 0, At, B0); PG8_MMA(1, 1, At, B1); PG8_BAR; PG8_SCHED;
;             PG8_LDB(B0, 1, 0); PG8_LDB(B1, 1, 1); PG8_SCHED; PG8_LDA(At, 1, 0); PG8_STAGEA(PG8_SA(0, 1), a2, 1, last);
;             PG8_WAIT_V(8); PG8_WAIT_L(0); PG8_BAR; PG8_MMA(0, 0, At, B0); PG8_MMA(0, 1, At, B1); PG8_BAR; PG8_SCHED;
;             PG8_LDA(At, 1, 1); PG8_STAGE(PG8_SB(1, 0), b3, voffB); PG8_STAGE(PG8_SB(1, 1), b3 + hstep, voffB); PG8_STAGEA(PG8_SA(1, 0), a3, 0, last);
;             PG8_WAIT_V(8); PG8_WAIT_L(0); PG8_BAR; PG8_MMA(1, 0, At, B0); PG8_MMA(1, 1, At, B1); PG8_BAR; PG8_SCHED;
.LBB0_110:
	v_add_u32_e32 v142, s79, v170
	v_add_u32_e32 v175, s80, v170
	ds_read_b128 v[130:133], v142
	ds_read_b128 v[134:137], v142 offset:1024
	ds_read_b128 v[138:141], v142 offset:2048
	ds_read_b128 v[142:145], v142 offset:3072
	ds_read_b128 v[162:165], v175
	ds_read_b128 v[166:169], v175 offset:1024
	ds_read_b128 v[176:179], v175 offset:2048
	ds_read_b128 v[180:183], v175 offset:3072
	s_add_u32 s54, s10, 0xfff80080
	s_addc_u32 s55, s11, -1
	s_cmp_eq_u32 s49, 28
	s_cselect_b32 s61, s9, s55
	s_cselect_b32 s60, s18, s54
	s_cselect_b32 s55, s19, s47
	s_cselect_b32 s54, s36, s37
	v_lshl_add_u64 v[200:201], s[10:11], 0, v[154:155]
	s_add_i32 m0, s57, 0xc000
	ds_read_b128 v[184:187], v174
	ds_read_b128 v[188:191], v174 offset:1024
	ds_read_b128 v[192:195], v174 offset:2048
	ds_read_b128 v[196:199], v174 offset:3072
	ds_read_b128 v[204:207], v174 offset:4096
	ds_read_b128 v[208:211], v174 offset:5120
	ds_read_b128 v[212:215], v174 offset:6144
	ds_read_b128 v[216:219], v174 offset:7168
	global_load_lds_dwordx4 v[200:201], off
	v_lshl_add_u64 v[200:201], s[10:11], 0, v[156:157]
	s_add_i32 m0, s57, 0xe000
	s_nop 0
	global_load_lds_dwordx4 v[200:201], off
	s_waitcnt vmcnt(8)
	s_waitcnt lgkmcnt(0)
	s_barrier
	s_setprio 1
	v_mfma_f32_16x16x32_bf16 v[114:117], v[130:133], v[184:187], v[114:117]
	v_mfma_f32_16x16x32_bf16 v[118:121], v[138:141], v[184:187], v[118:121]
	v_mfma_f32_16x16x32_bf16 v[98:101], v[130:133], v[192:195], v[98:101]
	v_mfma_f32_16x16x32_bf16 v[102:105], v[138:141], v[192:195], v[102:105]
	v_mfma_f32_16x16x32_bf16 v[82:85], v[130:133], v[204:207], v[82:85]
	v_mfma_f32_16x16x32_bf16 v[86:89], v[138:141], v[204:207], v[86:89]
	v_mfma_f32_16x16x32_bf16 v[66:69], v[130:133], v[212:215], v[66:69]
	v_mfma_f32_16x16x32_bf16 v[70:73], v[138:141], v[212:215], v[70:73]
	v_mfma_f32_16x16x32_bf16 v[114:117], v[134:137], v[188:191], v[114:117]
	v_mfma_f32_16x16x32_bf16 v[118:121], v[142:145], v[188:191], v[118:121]
	v_mfma_f32_16x16x32_bf16 v[98:101], v[134:137], v[196:199], v[98:101]
	v_mfma_f32_16x16x32_bf16 v[102:105], v[142:145], v[196:199], v[102:105]
	v_mfma_f32_16x16x32_bf16 v[82:85], v[134:137], v[208:211], v[82:85]
	v_mfma_f32_16x16x32_bf16 v[86:89], v[142:145], v[208:211], v[86:89]
	v_mfma_f32_16x16x32_bf16 v[66:69], v[134:137], v[216:219], v[66:69]
	v_mfma_f32_16x16x32_bf16 v[70:73], v[142:145], v[216:219], v[70:73]
	v_mfma_f32_16x16x32_bf16 v[122:125], v[162:165], v[184:187], v[122:125]
	v_mfma_f32_16x16x32_bf16 v[126:129], v[176:179], v[184:187], v[126:129]
	v_mfma_f32_16x16x32_bf16 v[106:109], v[162:165], v[192:195], v[106:109]
	v_mfma_f32_16x16x32_bf16 v[110:113], v[176:179], v[192:195], v[110:113]
	v_mfma_f32_16x16x32_bf16 v[90:93], v[162:165], v[204:207], v[90:93]
	v_mfma_f32_16x16x32_bf16 v[94:97], v[176:179], v[204:207], v[94:97]
	v_mfma_f32_16x16x32_bf16 v[74:77], v[162:165], v[212:215], v[74:77]
	v_mfma_f32_16x16x32_bf16 v[78:81], v[176:179], v[212:215], v[78:81]
	v_mfma_f32_16x16x32_bf16 v[122:125], v[166:169], v[188:191], v[122:125]
	v_mfma_f32_16x16x32_bf16 v[126:129], v[180:183], v[188:191], v[126:129]
	v_mfma_f32_16x16x32_bf16 v[106:109], v[166:169], v[196:199], v[106:109]
	v_mfma_f32_16x16x32_bf16 v[110:113], v[180:183], v[196:199], v[110:113]
	v_mfma_f32_16x16x32_bf16 v[90:93], v[166:169], v[208:211], v[90:93]
	v_mfma_f32_16x16x32_bf16 v[94:97], v[180:183], v[208:211], v[94:97]
	v_mfma_f32_16x16x32_bf16 v[74:77], v[166:169], v[216:219], v[74:77]
	v_mfma_f32_16x16x32_bf16 v[78:81], v[180:183], v[216:219], v[78:81]
	s_setprio 0
	s_barrier
	s_add_i32 s59, s79, s66
	v_lshl_add_u64 v[200:201], s[54:55], 0, v[148:149]
	s_mov_b32 m0, s59
	ds_read_b128 v[184:187], v174 offset:16384
	ds_read_b128 v[188:191], v174 offset:17408
	ds_read_b128 v[192:195], v174 offset:18432
	ds_read_b128 v[196:199], v174 offset:19456
	ds_read_b128 v[204:207], v174 offset:20480
	ds_read_b128 v[208:211], v174 offset:21504
	ds_read_b128 v[212:215], v174 offset:22528
	ds_read_b128 v[216:219], v174 offset:23552
	global_load_lds_dwordx4 v[200:201], off
	s_add_i32 m0, s59, 0x2000
	s_add_u32 s62, s54, 0x80000
	v_lshl_add_u64 v[220:221], s[54:55], 0, v[152:153]
	s_addc_u32 s63, s55, 0
	s_add_i32 s59, s80, s66
	global_load_lds_dwordx4 v[220:221], off
	v_lshl_add_u64 v[222:223], s[62:63], 0, v[148:149]
	s_mov_b32 m0, s59
	v_lshl_add_u64 v[224:225], s[60:61], 0, v[150:151]
	global_load_lds_dwordx4 v[222:223], off
	v_lshl_add_u64 v[222:223], s[62:63], 0, v[152:153]
	s_add_i32 m0, s59, 0x2000
	s_nop 0
	global_load_lds_dwordx4 v[222:223], off
	v_lshl_add_u64 v[222:223], s[60:61], 0, v[146:147]
	s_mov_b32 m0, s57
	s_nop 0
	global_load_lds_dwordx4 v[222:223], off
	s_mov_b32 m0, s67
	s_nop 0
	global_load_lds_dwordx4 v[224:225], off
	s_waitcnt vmcnt(8)
	s_waitcnt lgkmcnt(0)
	s_barrier
; #define PG8_STAGE(bufoff, gbase, voff) do { _Pragma("unroll") for (int _i = 0; _i < 2; ++_i) \
;         __builtin_amdgcn_global_load_lds((const unsigned*)((const char*)(gbase) + (voff)[_i]), (PG8_LAS unsigned*)(lds + (bufoff) + ldsw + _i * 8192), 16, 0, 0); } while (0)
; #define PG8_LDA(dst, b, h) do { _Pragma("unroll") for (int m = 0; m < 4; ++m) _Pragma("unroll") for (int k = 0; k < 2; ++k) dst[m][k] = *(const PG8_LAS bf16x8*)(lds + PG8_SA(b, h) + aoff + m * 2048 + k * 1024); } while (0)
; #define PG8_LDB(dst, b, h) do { _Pragma("unroll") for (int n = 0; n < 2; ++n) _Pragma("unroll") for (int k = 0; k < 2; ++k) dst[n][k] = *(const PG8_LAS bf16x8*)(lds + PG8_SB(b, h) + boff + n * 2048 + k * 1024); } while (0)
; #define PG8_MMA(ai, bj, At, Bt) do { __builtin_amdgcn_s_setprio(1); _Pragma("unroll") for (int m = 0; m < 4; ++m) _Pragma("unroll") for (int n = 0; n < 2; ++n) _Pragma("unroll") for (int k = 0; k < 2; ++k) \
;         acc[ai][bj][m][n] = __builtin_amdgcn_mfma_f32_16x16x32_bf16(Bt[n][k], At[m][k], acc[ai][bj][m][n], 0, 0, 0); __builtin_amdgcn_s_setprio(0); } while (0)
; #define PG8_WAIT_V(n) asm volatile("s_waitcnt vmcnt(" #n ")" ::: "memory")
; #define PG8_WAIT_L(n) asm volatile("s_waitcnt lgkmcnt(" #n ")" ::: "memory")
; #define PG8_BAR __builtin_amdgcn_s_barrier()
; #define PG8_SCHED __builtin_amdgcn_sched_barrier(0)
; template <class Epi, class Sched, bool ALIGN_EPI = false, bool SP2 = false>
; __device__ __forceinline__ void gemm_phase(PG8_LAS unsigned char* lds, const Gemm g, const Sched& S, const Epi& E) {
;     ...
;             PG8_LDA(At, 0, 1); PG8_STAGE(PG8_SB(0, 0), b2, voffB); PG8_STAGE(PG8_SB(0, 1), b2 + hstep, voffB); PG8_STAGEA(PG8_SA(0, 0), a2, 0, last);
;             PG8_WAIT_V(8); PG8_WAIT_L(0); PG8_BAR; PG8_MMA(1, 0, At, B0); PG8_MMA(1, 1, At, B1); PG8_BAR; PG8_SCHED;
;             PG8_LDB(B0, 1, 0); PG8_LDB(B1, 1, 1); PG8_SCHED; PG8_LDA(At, 1, 0); PG8_STAGEA(PG8_SA(0, 1), a2, 1, last);
;             PG8_WAIT_V(8); PG8_WAIT_L(0); PG8_BAR; PG8_MMA(0, 0, At, B0); PG8_MMA(0, 1, At, B1); PG8_BAR; PG8_SCHED;
	s_setprio 1
	v_mfma_f32_16x16x32_bf16 v[58:61], v[130:133], v[184:187], v[58:61]
	v_mfma_f32_16x16x32_bf16 v[62:65], v[138:141], v[184:187], v[62:65]
	v_mfma_f32_16x16x32_bf16 v[42:45], v[130:133], v[192:195], v[42:45]
	v_mfma_f32_16x16x32_bf16 v[46:49], v[138:141], v[192:195], v[46:49]
	v_mfma_f32_16x16x32_bf16 v[18:21], v[130:133], v[204:207], v[18:21]
	v_mfma_f32_16x16x32_bf16 v[22:25], v[138:141], v[204:207], v[22:25]
	v_mfma_f32_16x16x32_bf16 v[6:9], v[130:133], v[212:215], v[6:9]
	v_mfma_f32_16x16x32_bf16 v[14:17], v[138:141], v[212:215], v[14:17]
	v_mfma_f32_16x16x32_bf16 v[58:61], v[134:137], v[188:191], v[58:61]
	v_mfma_f32_16x16x32_bf16 v[62:65], v[142:145], v[188:191], v[62:65]
	v_mfma_f32_16x16x32_bf16 v[42:45], v[134:137], v[196:199], v[42:45]
	v_mfma_f32_16x16x32_bf16 v[46:49], v[142:145], v[196:199], v[46:49]
	v_mfma_f32_16x16x32_bf16 v[18:21], v[134:137], v[208:211], v[18:21]
	v_mfma_f32_16x16x32_bf16 v[22:25], v[142:145], v[208:211], v[22:25]
	v_mfma_f32_16x16x32_bf16 v[6:9], v[134:137], v[216:219], v[6:9]
	v_mfma_f32_16x16x32_bf16 v[14:17], v[142:145], v[216:219], v[14:17]
	v_mfma_f32_16x16x32_bf16 v[50:53], v[162:165], v[184:187], v[50:53]
	v_mfma_f32_16x16x32_bf16 v[54:57], v[176:179], v[184:187], v[54:57]
	v_mfma_f32_16x16x32_bf16 v[34:37], v[162:165], v[192:195], v[34:37]
	v_mfma_f32_16x16x32_bf16 v[38:41], v[176:179], v[192:195], v[38:41]
	v_mfma_f32_16x16x32_bf16 v[26:29], v[162:165], v[204:207], v[26:29]
	v_mfma_f32_16x16x32_bf16 v[30:33], v[176:179], v[204:207], v[30:33]
	v_mfma_f32_16x16x32_bf16 v[10:13], v[162:165], v[212:215], v[10:13]
	v_mfma_f32_16x16x32_bf16 v[2:5], v[176:179], v[212:215], v[2:5]
	v_mfma_f32_16x16x32_bf16 v[50:53], v[166:169], v[188:191], v[50:53]
	v_mfma_f32_16x16x32_bf16 v[54:57], v[180:183], v[188:191], v[54:57]
	v_mfma_f32_16x16x32_bf16 v[34:37], v[166:169], v[196:199], v[34:37]
	v_mfma_f32_16x16x32_bf16 v[38:41], v[180:183], v[196:199], v[38:41]
	v_mfma_f32_16x16x32_bf16 v[26:29], v[166:169], v[208:211], v[26:29]
	v_mfma_f32_16x16x32_bf16 v[30:33], v[180:183], v[208:211], v[30:33]
	v_mfma_f32_16x16x32_bf16 v[10:13], v[166:169], v[216:219], v[10:13]
	v_mfma_f32_16x16x32_bf16 v[2:5], v[180:183], v[216:219], v[2:5]
	s_setprio 0
	s_barrier
	s_add_i32 s59, 0, 0x18000
	s_add_i32 s62, 0, 0x1c000
	v_add_u32_e32 v142, s59, v170
	v_add_u32_e32 v175, s62, v170
	ds_read_b128 v[130:133], v142
	ds_read_b128 v[134:137], v142 offset:1024
	ds_read_b128 v[138:141], v142 offset:2048
	ds_read_b128 v[142:145], v142 offset:3072
	ds_read_b128 v[162:165], v175
	ds_read_b128 v[166:169], v175 offset:1024
	ds_read_b128 v[176:179], v175 offset:2048
	ds_read_b128 v[180:183], v175 offset:3072
	s_add_u32 s60, s60, 0x80000
	s_addc_u32 s61, s61, 0
	s_mov_b32 m0, s68
	v_lshl_add_u64 v[226:227], s[60:61], 0, v[146:147]
	ds_read_b128 v[184:187], v174 offset:32768
	ds_read_b128 v[188:191], v174 offset:33792
	ds_read_b128 v[192:195], v174 offset:34816
	ds_read_b128 v[196:199], v174 offset:35840
	ds_read_b128 v[204:207], v174 offset:36864
	ds_read_b128 v[208:211], v174 offset:37888
	ds_read_b128 v[212:215], v174 offset:38912
	ds_read_b128 v[216:219], v174 offset:39936
	global_load_lds_dwordx4 v[226:227], off
	v_lshl_add_u64 v[226:227], s[60:61], 0, v[150:151]
	s_mov_b32 m0, s69
	s_nop 0
	global_load_lds_dwordx4 v[226:227], off
	s_waitcnt vmcnt(8)
	s_waitcnt lgkmcnt(0)
	s_barrier
	s_setprio 1
	v_mfma_f32_16x16x32_bf16 v[114:117], v[130:133], v[184:187], v[114:117]
	v_mfma_f32_16x16x32_bf16 v[118:121], v[138:141], v[184:187], v[118:121]
	v_mfma_f32_16x16x32_bf16 v[98:101], v[130:133], v[192:195], v[98:101]
	v_mfma_f32_16x16x32_bf16 v[102:105], v[138:141], v[192:195], v[102:105]
	v_mfma_f32_16x16x32_bf16 v[82:85], v[130:133], v[204:207], v[82:85]
	v_mfma_f32_16x16x32_bf16 v[86:89], v[138:141], v[204:207], v[86:89]
	v_mfma_f32_16x16x32_bf16 v[66:69], v[130:133], v[212:215], v[66:69]
	v_mfma_f32_16x16x32_bf16 v[70:73], v[138:141], v[212:215], v[70:73]
	v_mfma_f32_16x16x32_bf16 v[114:117], v[134:137], v[188:191], v[114:117]
	v_mfma_f32_16x16x32_bf16 v[118:121], v[142:145], v[188:191], v[118:121]
	v_mfma_f32_16x16x32_bf16 v[98:101], v[134:137], v[196:199], v[98:101]
	v_mfma_f32_16x16x32_bf16 v[102:105], v[142:145], v[196:199], v[102:105]
	v_mfma_f32_16x16x32_bf16 v[82:85], v[134:137], v[208:211], v[82:85]
	v_mfma_f32_16x16x32_bf16 v[86:89], v[142:145], v[208:211], v[86:89]
	v_mfma_f32_16x16x32_bf16 v[66:69], v[134:137], v[216:219], v[66:69]
	v_mfma_f32_16x16x32_bf16 v[70:73], v[142:145], v[216:219], v[70:73]
	v_mfma_f32_16x16x32_bf16 v[122:125], v[162:165], v[184:187], v[122:125]
	v_mfma_f32_16x16x32_bf16 v[126:129], v[176:179], v[184:187], v[126:129]
	v_mfma_f32_16x16x32_bf16 v[106:109], v[162:165], v[192:195], v[106:109]
	v_mfma_f32_16x16x32_bf16 v[110:113], v[176:179], v[192:195], v[110:113]
	v_mfma_f32_16x16x32_bf16 v[90:93], v[162:165], v[204:207], v[90:93]
	v_mfma_f32_16x16x32_bf16 v[94:97], v[176:179], v[204:207], v[94:97]
	v_mfma_f32_16x16x32_bf16 v[74:77], v[162:165], v[212:215], v[74:77]
	v_mfma_f32_16x16x32_bf16 v[78:81], v[176:179], v[212:215], v[78:81]
	v_mfma_f32_16x16x32_bf16 v[122:125], v[166:169], v[188:191], v[122:125]
	v_mfma_f32_16x16x32_bf16 v[126:129], v[180:183], v[188:191], v[126:129]
	v_mfma_f32_16x16x32_bf16 v[106:109], v[166:169], v[196:199], v[106:109]
	v_mfma_f32_16x16x32_bf16 v[110:113], v[180:183], v[196:199], v[110:113]
	v_mfma_f32_16x16x32_bf16 v[90:93], v[166:169], v[208:211], v[90:93]
	v_mfma_f32_16x16x32_bf16 v[94:97], v[180:183], v[208:211], v[94:97]
	v_mfma_f32_16x16x32_bf16 v[74:77], v[166:169], v[216:219], v[74:77]
	v_mfma_f32_16x16x32_bf16 v[78:81], v[180:183], v[216:219], v[78:81]
	s_setprio 0
	s_barrier
; #define PG8_STAGE(bufoff, gbase, voff) do { _Pragma("unroll") for (int _i = 0; _i < 2; ++_i) \
;         __builtin_amdgcn_global_load_lds((const unsigned*)((const char*)(gbase) + (voff)[_i]), (PG8_LAS unsigned*)(lds + (bufoff) + ldsw + _i * 8192), 16, 0, 0); } while (0)
; #define PG8_LDA(dst, b, h) do { _Pragma("unroll") for (int m = 0; m < 4; ++m) _Pragma("unroll") for (int k = 0; k < 2; ++k) dst[m][k] = *(const PG8_LAS bf16x8*)(lds + PG8_SA(b, h) + aoff + m * 2048 + k * 1024); } while (0)
; #define PG8_MMA(ai, bj, At, Bt) do { __builtin_amdgcn_s_setprio(1); _Pragma("unroll") for (int m = 0; m < 4; ++m) _Pragma("unroll") for (int n = 0; n < 2; ++n) _Pragma("unroll") for (int k = 0; k < 2; ++k) \
;         acc[ai][bj][m][n] = __builtin_amdgcn_mfma_f32_16x16x32_bf16(Bt[n][k], At[m][k], acc[ai][bj][m][n], 0, 0, 0); __builtin_amdgcn_s_setprio(0); } while (0)
; #define PG8_WAIT_V(n) asm volatile("s_waitcnt vmcnt(" #n ")" ::: "memory")
; #define PG8_WAIT_L(n) asm volatile("s_waitcnt lgkmcnt(" #n ")" ::: "memory")
; #define PG8_BAR __builtin_amdgcn_s_barrier()
; #define PG8_SCHED __builtin_amdgcn_sched_barrier(0)
; template <class Epi, class Sched, bool ALIGN_EPI = false, bool SP2 = false>
; __device__ __forceinline__ void gemm_phase(PG8_LAS unsigned char* lds, const Gemm g, const Sched& S, const Epi& E) {
;     ...
;         for (; t < tend; t += 2) {
;             const bool last = (t == nt - 2);
;             const char* a1 = cA + (size_t)(t + 1) * kstep;
;             const char* a2 = last ? nA : cA + (size_t)(t + 2) * kstep; const char* b2 = last ? nB : cB + (size_t)(t + 2) * kstep;
;     ...
;             PG8_LDA(At, 1, 1); PG8_STAGE(PG8_SB(1, 0), b3, voffB); PG8_STAGE(PG8_SB(1, 1), b3 + hstep, voffB); PG8_STAGEA(PG8_SA(1, 0), a3, 0, last);
;             PG8_WAIT_V(8); PG8_WAIT_L(0); PG8_BAR; PG8_MMA(1, 0, At, B0); PG8_MMA(1, 1, At, B1); PG8_BAR; PG8_SCHED;
	s_add_i32 s59, s59, s66
	v_lshl_add_u64 v[200:201], v[200:201], 0, s[26:27]
	s_mov_b32 m0, s59
	ds_read_b128 v[184:187], v174 offset:49152
	ds_read_b128 v[188:191], v174 offset:50176
	ds_read_b128 v[192:195], v174 offset:51200
	ds_read_b128 v[196:199], v174 offset:52224
	ds_read_b128 v[204:207], v174 offset:53248
	ds_read_b128 v[208:211], v174 offset:54272
	ds_read_b128 v[212:215], v174 offset:55296
	ds_read_b128 v[216:219], v174 offset:56320
	global_load_lds_dwordx4 v[200:201], off
	s_add_i32 m0, s59, 0x2000
	s_add_u32 s54, s54, 0x80080
	v_lshl_add_u64 v[200:201], v[220:221], 0, s[26:27]
	s_addc_u32 s55, s55, 0
	s_add_i32 s59, s62, s66
	global_load_lds_dwordx4 v[200:201], off
	v_lshl_add_u64 v[200:201], s[54:55], 0, v[148:149]
	s_mov_b32 m0, s59
	s_nop 0
	global_load_lds_dwordx4 v[200:201], off
	v_lshl_add_u64 v[200:201], s[54:55], 0, v[152:153]
	s_add_i32 m0, s59, 0x2000
	s_nop 0
	global_load_lds_dwordx4 v[200:201], off
	v_lshl_add_u64 v[200:201], v[222:223], 0, s[26:27]
	s_mov_b32 m0, s74
	s_nop 0
	global_load_lds_dwordx4 v[200:201], off
	v_lshl_add_u64 v[200:201], v[224:225], 0, s[26:27]
	s_mov_b32 m0, s75
	s_nop 0
	global_load_lds_dwordx4 v[200:201], off
	s_waitcnt vmcnt(8)
	s_waitcnt lgkmcnt(0)
	s_barrier
	s_setprio 1
	v_mfma_f32_16x16x32_bf16 v[58:61], v[130:133], v[184:187], v[58:61]
	v_mfma_f32_16x16x32_bf16 v[62:65], v[138:141], v[184:187], v[62:65]
	v_mfma_f32_16x16x32_bf16 v[42:45], v[130:133], v[192:195], v[42:45]
	v_mfma_f32_16x16x32_bf16 v[46:49], v[138:141], v[192:195], v[46:49]
	v_mfma_f32_16x16x32_bf16 v[18:21], v[130:133], v[204:207], v[18:21]
	v_mfma_f32_16x16x32_bf16 v[22:25], v[138:141], v[204:207], v[22:25]
	v_mfma_f32_16x16x32_bf16 v[6:9], v[130:133], v[212:215], v[6:9]
	v_mfma_f32_16x16x32_bf16 v[14:17], v[138:141], v[212:215], v[14:17]
	v_mfma_f32_16x16x32_bf16 v[58:61], v[134:137], v[188:191], v[58:61]
	v_mfma_f32_16x16x32_bf16 v[62:65], v[142:145], v[188:191], v[62:65]
	v_mfma_f32_16x16x32_bf16 v[42:45], v[134:137], v[196:199], v[42:45]
	v_mfma_f32_16x16x32_bf16 v[46:49], v[142:145], v[196:199], v[46:49]
	v_mfma_f32_16x16x32_bf16 v[18:21], v[134:137], v[208:211], v[18:21]
	v_mfma_f32_16x16x32_bf16 v[22:25], v[142:145], v[208:211], v[22:25]
	v_mfma_f32_16x16x32_bf16 v[6:9], v[134:137], v[216:219], v[6:9]
	v_mfma_f32_16x16x32_bf16 v[14:17], v[142:145], v[216:219], v[14:17]
	v_mfma_f32_16x16x32_bf16 v[50:53], v[162:165], v[184:187], v[50:53]
	v_mfma_f32_16x16x32_bf16 v[54:57], v[176:179], v[184:187], v[54:57]
	v_mfma_f32_16x16x32_bf16 v[34:37], v[162:165], v[192:195], v[34:37]
	v_mfma_f32_16x16x32_bf16 v[38:41], v[176:179], v[192:195], v[38:41]
	v_mfma_f32_16x16x32_bf16 v[26:29], v[162:165], v[204:207], v[26:29]
	v_mfma_f32_16x16x32_bf16 v[30:33], v[176:179], v[204:207], v[30:33]
	v_mfma_f32_16x16x32_bf16 v[10:13], v[162:165], v[212:215], v[10:13]
	v_mfma_f32_16x16x32_bf16 v[2:5], v[176:179], v[212:215], v[2:5]
	v_mfma_f32_16x16x32_bf16 v[50:53], v[166:169], v[188:191], v[50:53]
	v_mfma_f32_16x16x32_bf16 v[54:57], v[180:183], v[188:191], v[54:57]
	v_mfma_f32_16x16x32_bf16 v[34:37], v[166:169], v[196:199], v[34:37]
	v_mfma_f32_16x16x32_bf16 v[38:41], v[180:183], v[196:199], v[38:41]
	v_mfma_f32_16x16x32_bf16 v[26:29], v[166:169], v[208:211], v[26:29]
	v_mfma_f32_16x16x32_bf16 v[30:33], v[180:183], v[208:211], v[30:33]
	v_mfma_f32_16x16x32_bf16 v[10:13], v[166:169], v[216:219], v[10:13]
	v_mfma_f32_16x16x32_bf16 v[2:5], v[180:183], v[216:219], v[2:5]
	s_setprio 0
	s_barrier
	s_add_i32 s49, s49, 2
	s_add_u32 s10, s10, 0x100
	s_addc_u32 s11, s11, 0
	s_add_u32 s37, s37, 0x100
	s_addc_u32 s47, s47, 0
	s_cmp_gt_u32 s49, 29
	s_cbranch_scc0 .LBB0_110
	s_and_b64 vcc, exec, s[38:39]
	s_cbranch_vccz .LBB0_113
	s_barrier

; #define PG8_STAGE(bufoff, gbase, voff) do { _Pragma("unroll") for (int _i = 0; _i < 2; ++_i) \
;         __builtin_amdgcn_global_load_lds((const unsigned*)((const char*)(gbase) + (voff)[_i]), (PG8_LAS unsigned*)(lds + (bufoff) + ldsw + _i * 8192), 16, 0, 0); } while (0)
; #define PG8_LDA(dst, b, h) do { _Pragma("unroll") for (int m = 0; m < 4; ++m) _Pragma("unroll") for (int k = 0; k < 2; ++k) dst[m][k] = *(const PG8_LAS bf16x8*)(lds + PG8_SA(b, h) + aoff + m * 2048 + k * 1024); } while (0)
; #define PG8_WAIT_V(n) asm volatile("s_waitcnt vmcnt(" #n ")" ::: "memory")
; template <class Epi, class Sched, bool ALIGN_EPI = false, bool SP2 = false>
; __device__ __forceinline__ void gemm_phase(PG8_LAS unsigned char* lds, const Gemm g, const Sched& S, const Epi& E) {
;     ...
;         for (int kh = 0; kh < NKH; ++kh) {
;         const int tend = (NKH == 2 && kh == 0) ? nt / 2 : nt;
; #pragma unroll 1
;         for (; t < tend; t += 2) {
;             const bool last = (t == nt - 2);
;             const char* a1 = cA + (size_t)(t + 1) * kstep;
;             const char* a2 = last ? nA : cA + (size_t)(t + 2) * kstep; const char* b2 = last ? nB : cB + (size_t)(t + 2) * kstep;
;             const char* a3 = a2 + kstep; const char* b3 = b2 + kstep;
;             if (last && has_next) S.a_ready(nxt);
;             if constexpr (SP2) {
;             PG8_LDB(B0, 0, 0); PG8_LDB(B1, 0, 1); PG8_SCHED; PG8_LDA(At, 0, 0); PG8_STAGEA(PG8_SA(1, 1), a1, 1, false);
;             PG8_WAIT_V(8); PG8_WAIT_L(0); PG8_BAR; PG8_MMA(0, 0, At, B0); PG8_MMA(0, 1, At, B1); PG8_BAR; PG8_SCHED;
;             PG8_LDA(At, 0, 1); PG8_STAGE(PG8_SB(0, 0), b2, voffB); PG8_STAGE(PG8_SB(0, 1), b2 + hstep, voffB); PG8_STAGEA(PG8_SA(0, 0), a2, 0, last);
;             PG8_WAIT_V(8); PG8_WAIT_L(0); PG8_BAR; PG8_MMA(1, 0, At, B0); PG8_MMA(1, 1, At, B1); PG8_BAR; PG8_SCHED;
;             PG8_LDB(B0, 1, 0); PG8_LDB(B1, 1, 1); PG8_SCHED; PG8_LDA(At, 1, 0); PG8_STAGEA(PG8_SA(0, 1), a2, 1, last);
;             PG8_WAIT_V(8); PG8_WAIT_L(0); PG8_BAR; PG8_MMA(0, 0, At, B0); PG8_MMA(0, 1, At, B1); PG8_BAR; PG8_SCHED;
;             PG8_LDA(At, 1, 1); PG8_STAGE(PG8_SB(1, 0), b3, voffB); PG8_STAGE(PG8_SB(1, 1), b3 + hstep, voffB); PG8_STAGEA(PG8_SA(1, 0), a3, 0, last);
;             PG8_WAIT_V(8); PG8_WAIT_L(0); PG8_BAR; PG8_MMA(1, 0, At, B0); PG8_MMA(1, 1, At, B1); PG8_BAR; PG8_SCHED;
.LBB0_383:
	v_add_u32_e32 v142, s79, v173
	v_add_u32_e32 v170, s80, v173
	ds_read_b128 v[130:133], v142
	ds_read_b128 v[134:137], v142 offset:1024
	ds_read_b128 v[138:141], v142 offset:2048
	ds_read_b128 v[142:145], v142 offset:3072
	ds_read_b128 v[146:149], v170
	ds_read_b128 v[150:153], v170 offset:1024
	ds_read_b128 v[154:157], v170 offset:2048
	ds_read_b128 v[176:179], v170 offset:3072
	s_add_i32 s58, s56, 1
	s_ashr_i32 s59, s58, 31
	s_mov_b32 s62, s56
	s_add_i32 s56, s56, 2
	s_lshl_b64 s[96:97], s[58:59], 7
	s_cmp_eq_u32 s62, 30
	s_cselect_b32 s63, s9, s36
	s_cselect_b32 s62, s49, s19
	s_cselect_b32 s59, s89, s57
	s_cselect_b32 s58, s90, s37
	s_add_u32 s95, s10, s96
	s_addc_u32 s97, s11, s97
	s_add_u32 s96, s95, 0x80000
	s_addc_u32 s97, s97, 0
	v_lshl_add_u64 v[170:171], s[96:97], 0, v[158:159]
	s_add_i32 m0, s66, 0xc000
	ds_read_b128 v[180:183], v174
	ds_read_b128 v[184:187], v174 offset:1024
	ds_read_b128 v[188:191], v174 offset:2048
	ds_read_b128 v[192:195], v174 offset:3072
	ds_read_b128 v[196:199], v174 offset:4096
	ds_read_b128 v[204:207], v174 offset:5120
	ds_read_b128 v[208:211], v174 offset:6144
	ds_read_b128 v[212:215], v174 offset:7168
	global_load_lds_dwordx4 v[170:171], off
	v_lshl_add_u64 v[170:171], s[96:97], 0, v[162:163]
	s_add_i32 m0, s66, 0xe000
	s_nop 0
	global_load_lds_dwordx4 v[170:171], off
	s_waitcnt vmcnt(8)
	s_waitcnt lgkmcnt(0)
	s_barrier
	s_setprio 1
	v_mfma_f32_16x16x32_bf16 v[118:121], v[130:133], v[180:183], v[118:121]
	v_mfma_f32_16x16x32_bf16 v[114:117], v[138:141], v[180:183], v[114:117]
	v_mfma_f32_16x16x32_bf16 v[102:105], v[130:133], v[188:191], v[102:105]
	v_mfma_f32_16x16x32_bf16 v[98:101], v[138:141], v[188:191], v[98:101]
	v_mfma_f32_16x16x32_bf16 v[86:89], v[130:133], v[196:199], v[86:89]
	v_mfma_f32_16x16x32_bf16 v[82:85], v[138:141], v[196:199], v[82:85]
	v_mfma_f32_16x16x32_bf16 v[70:73], v[130:133], v[208:211], v[70:73]
	v_mfma_f32_16x16x32_bf16 v[66:69], v[138:141], v[208:211], v[66:69]
	v_mfma_f32_16x16x32_bf16 v[118:121], v[134:137], v[184:187], v[118:121]
	v_mfma_f32_16x16x32_bf16 v[114:117], v[142:145], v[184:187], v[114:117]
	v_mfma_f32_16x16x32_bf16 v[102:105], v[134:137], v[192:195], v[102:105]
	v_mfma_f32_16x16x32_bf16 v[98:101], v[142:145], v[192:195], v[98:101]
	v_mfma_f32_16x16x32_bf16 v[86:89], v[134:137], v[204:207], v[86:89]
	v_mfma_f32_16x16x32_bf16 v[82:85], v[142:145], v[204:207], v[82:85]
	v_mfma_f32_16x16x32_bf16 v[70:73], v[134:137], v[212:215], v[70:73]
	v_mfma_f32_16x16x32_bf16 v[66:69], v[142:145], v[212:215], v[66:69]
	v_mfma_f32_16x16x32_bf16 v[126:129], v[146:149], v[180:183], v[126:129]
	v_mfma_f32_16x16x32_bf16 v[122:125], v[154:157], v[180:183], v[122:125]
	v_mfma_f32_16x16x32_bf16 v[110:113], v[146:149], v[188:191], v[110:113]
	v_mfma_f32_16x16x32_bf16 v[106:109], v[154:157], v[188:191], v[106:109]
	v_mfma_f32_16x16x32_bf16 v[94:97], v[146:149], v[196:199], v[94:97]
	v_mfma_f32_16x16x32_bf16 v[90:93], v[154:157], v[196:199], v[90:93]
	v_mfma_f32_16x16x32_bf16 v[78:81], v[146:149], v[208:211], v[78:81]
	v_mfma_f32_16x16x32_bf16 v[74:77], v[154:157], v[208:211], v[74:77]
	v_mfma_f32_16x16x32_bf16 v[126:129], v[150:153], v[184:187], v[126:129]
	v_mfma_f32_16x16x32_bf16 v[122:125], v[176:179], v[184:187], v[122:125]
	v_mfma_f32_16x16x32_bf16 v[110:113], v[150:153], v[192:195], v[110:113]
	v_mfma_f32_16x16x32_bf16 v[106:109], v[176:179], v[192:195], v[106:109]
	v_mfma_f32_16x16x32_bf16 v[94:97], v[150:153], v[204:207], v[94:97]
	v_mfma_f32_16x16x32_bf16 v[90:93], v[176:179], v[204:207], v[90:93]
	v_mfma_f32_16x16x32_bf16 v[78:81], v[150:153], v[212:215], v[78:81]
	v_mfma_f32_16x16x32_bf16 v[74:77], v[176:179], v[212:215], v[74:77]
	s_setprio 0
	s_barrier
	s_add_i32 s95, s79, s65
	v_lshl_add_u64 v[170:171], s[58:59], 0, v[160:161]
	s_mov_b32 m0, s95
	ds_read_b128 v[180:183], v174 offset:16384
	ds_read_b128 v[184:187], v174 offset:17408
	ds_read_b128 v[188:191], v174 offset:18432
	ds_read_b128 v[192:195], v174 offset:19456
	ds_read_b128 v[196:199], v174 offset:20480
	ds_read_b128 v[204:207], v174 offset:21504
	ds_read_b128 v[208:211], v174 offset:22528
	ds_read_b128 v[212:215], v174 offset:23552
	global_load_lds_dwordx4 v[170:171], off
	s_add_i32 m0, s95, 0x2000
	s_add_u32 s96, s58, 0x80000
	v_lshl_add_u64 v[200:201], s[58:59], 0, v[164:165]
	s_addc_u32 s97, s59, 0
	s_add_i32 s95, s80, s65
	global_load_lds_dwordx4 v[200:201], off
	v_lshl_add_u64 v[216:217], s[96:97], 0, v[160:161]
	s_mov_b32 m0, s95
	v_lshl_add_u64 v[218:219], s[62:63], 0, v[162:163]
	global_load_lds_dwordx4 v[216:217], off
	v_lshl_add_u64 v[216:217], s[96:97], 0, v[164:165]
	s_add_i32 m0, s95, 0x2000
	s_nop 0
	global_load_lds_dwordx4 v[216:217], off
	v_lshl_add_u64 v[216:217], s[62:63], 0, v[158:159]
	s_mov_b32 m0, s66
	s_nop 0
	global_load_lds_dwordx4 v[216:217], off
	s_mov_b32 m0, s67
	s_nop 0
	global_load_lds_dwordx4 v[218:219], off
	s_waitcnt vmcnt(8)
	s_waitcnt lgkmcnt(0)
	s_barrier
; #define PG8_STAGE(bufoff, gbase, voff) do { _Pragma("unroll") for (int _i = 0; _i < 2; ++_i) \
;         __builtin_amdgcn_global_load_lds((const unsigned*)((const char*)(gbase) + (voff)[_i]), (PG8_LAS unsigned*)(lds + (bufoff) + ldsw + _i * 8192), 16, 0, 0); } while (0)
; #define PG8_LDA(dst, b, h) do { _Pragma("unroll") for (int m = 0; m < 4; ++m) _Pragma("unroll") for (int k = 0; k < 2; ++k) dst[m][k] = *(const PG8_LAS bf16x8*)(lds + PG8_SA(b, h) + aoff + m * 2048 + k * 1024); } while (0)
; #define PG8_LDB(dst, b, h) do { _Pragma("unroll") for (int n = 0; n < 2; ++n) _Pragma("unroll") for (int k = 0; k < 2; ++k) dst[n][k] = *(const PG8_LAS bf16x8*)(lds + PG8_SB(b, h) + boff + n * 2048 + k * 1024); } while (0)
; #define PG8_MMA(ai, bj, At, Bt) do { __builtin_amdgcn_s_setprio(1); _Pragma("unroll") for (int m = 0; m < 4; ++m) _Pragma("unroll") for (int n = 0; n < 2; ++n) _Pragma("unroll") for (int k = 0; k < 2; ++k) \
;         acc[ai][bj][m][n] = __builtin_amdgcn_mfma_f32_16x16x32_bf16(Bt[n][k], At[m][k], acc[ai][bj][m][n], 0, 0, 0); __builtin_amdgcn_s_setprio(0); } while (0)
; #define PG8_WAIT_V(n) asm volatile("s_waitcnt vmcnt(" #n ")" ::: "memory")
; #define PG8_WAIT_L(n) asm volatile("s_waitcnt lgkmcnt(" #n ")" ::: "memory")
; #define PG8_BAR __builtin_amdgcn_s_barrier()
; #define PG8_SCHED __builtin_amdgcn_sched_barrier(0)
; template <class Epi, class Sched, bool ALIGN_EPI = false, bool SP2 = false>
; __device__ __forceinline__ void gemm_phase(PG8_LAS unsigned char* lds, const Gemm g, const Sched& S, const Epi& E) {
;     ...
;             PG8_LDA(At, 0, 1); PG8_STAGE(PG8_SB(0, 0), b2, voffB); PG8_STAGE(PG8_SB(0, 1), b2 + hstep, voffB); PG8_STAGEA(PG8_SA(0, 0), a2, 0, last);
;             PG8_WAIT_V(8); PG8_WAIT_L(0); PG8_BAR; PG8_MMA(1, 0, At, B0); PG8_MMA(1, 1, At, B1); PG8_BAR; PG8_SCHED;
;             PG8_LDB(B0, 1, 0); PG8_LDB(B1, 1, 1); PG8_SCHED; PG8_LDA(At, 1, 0); PG8_STAGEA(PG8_SA(0, 1), a2, 1, last);
;             PG8_WAIT_V(8); PG8_WAIT_L(0); PG8_BAR; PG8_MMA(0, 0, At, B0); PG8_MMA(0, 1, At, B1); PG8_BAR; PG8_SCHED;
	s_setprio 1
	v_mfma_f32_16x16x32_bf16 v[54:57], v[130:133], v[180:183], v[54:57]
	v_mfma_f32_16x16x32_bf16 v[50:53], v[138:141], v[180:183], v[50:53]
	v_mfma_f32_16x16x32_bf16 v[38:41], v[130:133], v[188:191], v[38:41]
	v_mfma_f32_16x16x32_bf16 v[34:37], v[138:141], v[188:191], v[34:37]
	v_mfma_f32_16x16x32_bf16 v[22:25], v[130:133], v[196:199], v[22:25]
	v_mfma_f32_16x16x32_bf16 v[18:21], v[138:141], v[196:199], v[18:21]
	v_mfma_f32_16x16x32_bf16 v[10:13], v[130:133], v[208:211], v[10:13]
	v_mfma_f32_16x16x32_bf16 v[6:9], v[138:141], v[208:211], v[6:9]
	v_mfma_f32_16x16x32_bf16 v[54:57], v[134:137], v[184:187], v[54:57]
	v_mfma_f32_16x16x32_bf16 v[50:53], v[142:145], v[184:187], v[50:53]
	v_mfma_f32_16x16x32_bf16 v[38:41], v[134:137], v[192:195], v[38:41]
	v_mfma_f32_16x16x32_bf16 v[34:37], v[142:145], v[192:195], v[34:37]
	v_mfma_f32_16x16x32_bf16 v[22:25], v[134:137], v[204:207], v[22:25]
	v_mfma_f32_16x16x32_bf16 v[18:21], v[142:145], v[204:207], v[18:21]
	v_mfma_f32_16x16x32_bf16 v[10:13], v[134:137], v[212:215], v[10:13]
	v_mfma_f32_16x16x32_bf16 v[6:9], v[142:145], v[212:215], v[6:9]
	v_mfma_f32_16x16x32_bf16 v[62:65], v[146:149], v[180:183], v[62:65]
	v_mfma_f32_16x16x32_bf16 v[58:61], v[154:157], v[180:183], v[58:61]
	v_mfma_f32_16x16x32_bf16 v[46:49], v[146:149], v[188:191], v[46:49]
	v_mfma_f32_16x16x32_bf16 v[42:45], v[154:157], v[188:191], v[42:45]
	v_mfma_f32_16x16x32_bf16 v[30:33], v[146:149], v[196:199], v[30:33]
	v_mfma_f32_16x16x32_bf16 v[26:29], v[154:157], v[196:199], v[26:29]
	v_mfma_f32_16x16x32_bf16 v[14:17], v[146:149], v[208:211], v[14:17]
	v_mfma_f32_16x16x32_bf16 v[2:5], v[154:157], v[208:211], v[2:5]
	v_mfma_f32_16x16x32_bf16 v[62:65], v[150:153], v[184:187], v[62:65]
	v_mfma_f32_16x16x32_bf16 v[58:61], v[176:179], v[184:187], v[58:61]
	v_mfma_f32_16x16x32_bf16 v[46:49], v[150:153], v[192:195], v[46:49]
	v_mfma_f32_16x16x32_bf16 v[42:45], v[176:179], v[192:195], v[42:45]
	v_mfma_f32_16x16x32_bf16 v[30:33], v[150:153], v[204:207], v[30:33]
	v_mfma_f32_16x16x32_bf16 v[26:29], v[176:179], v[204:207], v[26:29]
	v_mfma_f32_16x16x32_bf16 v[14:17], v[150:153], v[212:215], v[14:17]
	v_mfma_f32_16x16x32_bf16 v[2:5], v[176:179], v[212:215], v[2:5]
	s_setprio 0
	s_barrier
	s_add_i32 s95, 0, 0x18000
	s_add_i32 s96, 0, 0x1c000
	v_add_u32_e32 v142, s95, v173
	v_add_u32_e32 v175, s96, v173
	ds_read_b128 v[130:133], v142
	ds_read_b128 v[134:137], v142 offset:1024
	ds_read_b128 v[138:141], v142 offset:2048
	ds_read_b128 v[142:145], v142 offset:3072
	ds_read_b128 v[146:149], v175
	ds_read_b128 v[150:153], v175 offset:1024
	ds_read_b128 v[154:157], v175 offset:2048
	ds_read_b128 v[176:179], v175 offset:3072
	s_add_u32 s62, s62, 0x80000
	s_addc_u32 s63, s63, 0
	s_mov_b32 m0, s68
	v_lshl_add_u64 v[220:221], s[62:63], 0, v[158:159]
	ds_read_b128 v[180:183], v174 offset:32768
	ds_read_b128 v[184:187], v174 offset:33792
	ds_read_b128 v[188:191], v174 offset:34816
	ds_read_b128 v[192:195], v174 offset:35840
	ds_read_b128 v[196:199], v174 offset:36864
	ds_read_b128 v[204:207], v174 offset:37888
	ds_read_b128 v[208:211], v174 offset:38912
	ds_read_b128 v[212:215], v174 offset:39936
	global_load_lds_dwordx4 v[220:221], off
	v_lshl_add_u64 v[220:221], s[62:63], 0, v[162:163]
	s_mov_b32 m0, s69
	s_nop 0
	global_load_lds_dwordx4 v[220:221], off
	s_waitcnt vmcnt(8)
	s_waitcnt lgkmcnt(0)
	s_barrier
	s_setprio 1
	v_mfma_f32_16x16x32_bf16 v[118:121], v[130:133], v[180:183], v[118:121]
	v_mfma_f32_16x16x32_bf16 v[114:117], v[138:141], v[180:183], v[114:117]
	v_mfma_f32_16x16x32_bf16 v[102:105], v[130:133], v[188:191], v[102:105]
	v_mfma_f32_16x16x32_bf16 v[98:101], v[138:141], v[188:191], v[98:101]
	v_mfma_f32_16x16x32_bf16 v[86:89], v[130:133], v[196:199], v[86:89]
	v_mfma_f32_16x16x32_bf16 v[82:85], v[138:141], v[196:199], v[82:85]
	v_mfma_f32_16x16x32_bf16 v[70:73], v[130:133], v[208:211], v[70:73]
	v_mfma_f32_16x16x32_bf16 v[66:69], v[138:141], v[208:211], v[66:69]
	v_mfma_f32_16x16x32_bf16 v[118:121], v[134:137], v[184:187], v[118:121]
	v_mfma_f32_16x16x32_bf16 v[114:117], v[142:145], v[184:187], v[114:117]
	v_mfma_f32_16x16x32_bf16 v[102:105], v[134:137], v[192:195], v[102:105]
	v_mfma_f32_16x16x32_bf16 v[98:101], v[142:145], v[192:195], v[98:101]
	v_mfma_f32_16x16x32_bf16 v[86:89], v[134:137], v[204:207], v[86:89]
	v_mfma_f32_16x16x32_bf16 v[82:85], v[142:145], v[204:207], v[82:85]
	v_mfma_f32_16x16x32_bf16 v[70:73], v[134:137], v[212:215], v[70:73]
	v_mfma_f32_16x16x32_bf16 v[66:69], v[142:145], v[212:215], v[66:69]
	v_mfma_f32_16x16x32_bf16 v[126:129], v[146:149], v[180:183], v[126:129]
	v_mfma_f32_16x16x32_bf16 v[122:125], v[154:157], v[180:183], v[122:125]
	v_mfma_f32_16x16x32_bf16 v[110:113], v[146:149], v[188:191], v[110:113]
	v_mfma_f32_16x16x32_bf16 v[106:109], v[154:157], v[188:191], v[106:109]
	v_mfma_f32_16x16x32_bf16 v[94:97], v[146:149], v[196:199], v[94:97]
	v_mfma_f32_16x16x32_bf16 v[90:93], v[154:157], v[196:199], v[90:93]
	v_mfma_f32_16x16x32_bf16 v[78:81], v[146:149], v[208:211], v[78:81]
	v_mfma_f32_16x16x32_bf16 v[74:77], v[154:157], v[208:211], v[74:77]
	v_mfma_f32_16x16x32_bf16 v[126:129], v[150:153], v[184:187], v[126:129]
	v_mfma_f32_16x16x32_bf16 v[122:125], v[176:179], v[184:187], v[122:125]
	v_mfma_f32_16x16x32_bf16 v[110:113], v[150:153], v[192:195], v[110:113]
	v_mfma_f32_16x16x32_bf16 v[106:109], v[176:179], v[192:195], v[106:109]
	v_mfma_f32_16x16x32_bf16 v[94:97], v[150:153], v[204:207], v[94:97]
	v_mfma_f32_16x16x32_bf16 v[90:93], v[176:179], v[204:207], v[90:93]
	v_mfma_f32_16x16x32_bf16 v[78:81], v[150:153], v[212:215], v[78:81]
	v_mfma_f32_16x16x32_bf16 v[74:77], v[176:179], v[212:215], v[74:77]
	s_setprio 0
	s_barrier
; #define PG8_STAGE(bufoff, gbase, voff) do { _Pragma("unroll") for (int _i = 0; _i < 2; ++_i) \
;         __builtin_amdgcn_global_load_lds((const unsigned*)((const char*)(gbase) + (voff)[_i]), (PG8_LAS unsigned*)(lds + (bufoff) + ldsw + _i * 8192), 16, 0, 0); } while (0)
; #define PG8_LDA(dst, b, h) do { _Pragma("unroll") for (int m = 0; m < 4; ++m) _Pragma("unroll") for (int k = 0; k < 2; ++k) dst[m][k] = *(const PG8_LAS bf16x8*)(lds + PG8_SA(b, h) + aoff + m * 2048 + k * 1024); } while (0)
; #define PG8_MMA(ai, bj, At, Bt) do { __builtin_amdgcn_s_setprio(1); _Pragma("unroll") for (int m = 0; m < 4; ++m) _Pragma("unroll") for (int n = 0; n < 2; ++n) _Pragma("unroll") for (int k = 0; k < 2; ++k) \
;         acc[ai][bj][m][n] = __builtin_amdgcn_mfma_f32_16x16x32_bf16(Bt[n][k], At[m][k], acc[ai][bj][m][n], 0, 0, 0); __builtin_amdgcn_s_setprio(0); } while (0)
; #define PG8_WAIT_V(n) asm volatile("s_waitcnt vmcnt(" #n ")" ::: "memory")
; #define PG8_WAIT_L(n) asm volatile("s_waitcnt lgkmcnt(" #n ")" ::: "memory")
; #define PG8_BAR __builtin_amdgcn_s_barrier()
; #define PG8_SCHED __builtin_amdgcn_sched_barrier(0)
; template <class Epi, class Sched, bool ALIGN_EPI = false, bool SP2 = false>
; __device__ __forceinline__ void gemm_phase(PG8_LAS unsigned char* lds, const Gemm g, const Sched& S, const Epi& E) {
;     ...
;         for (; t < tend; t += 2) {
;             const bool last = (t == nt - 2);
;             const char* a1 = cA + (size_t)(t + 1) * kstep;
;             const char* a2 = last ? nA : cA + (size_t)(t + 2) * kstep; const char* b2 = last ? nB : cB + (size_t)(t + 2) * kstep;
;     ...
;             PG8_LDA(At, 1, 1); PG8_STAGE(PG8_SB(1, 0), b3, voffB); PG8_STAGE(PG8_SB(1, 1), b3 + hstep, voffB); PG8_STAGEA(PG8_SA(1, 0), a3, 0, last);
;             PG8_WAIT_V(8); PG8_WAIT_L(0); PG8_BAR; PG8_MMA(1, 0, At, B0); PG8_MMA(1, 1, At, B1); PG8_BAR; PG8_SCHED;
	s_add_i32 s62, s95, s65
	v_lshl_add_u64 v[170:171], v[170:171], 0, s[26:27]
	s_mov_b32 m0, s62
	ds_read_b128 v[180:183], v174 offset:49152
	ds_read_b128 v[184:187], v174 offset:50176
	ds_read_b128 v[188:191], v174 offset:51200
	ds_read_b128 v[192:195], v174 offset:52224
	ds_read_b128 v[196:199], v174 offset:53248
	ds_read_b128 v[204:207], v174 offset:54272
	ds_read_b128 v[208:211], v174 offset:55296
	ds_read_b128 v[212:215], v174 offset:56320
	global_load_lds_dwordx4 v[170:171], off
	s_add_i32 m0, s62, 0x2000
	s_add_u32 s58, s58, 0x80080
	v_lshl_add_u64 v[170:171], v[200:201], 0, s[26:27]
	s_addc_u32 s59, s59, 0
	s_add_i32 s62, s96, s65
	global_load_lds_dwordx4 v[170:171], off
	v_lshl_add_u64 v[170:171], s[58:59], 0, v[160:161]
	s_mov_b32 m0, s62
	s_nop 0
	global_load_lds_dwordx4 v[170:171], off
	v_lshl_add_u64 v[170:171], s[58:59], 0, v[164:165]
	s_add_i32 m0, s62, 0x2000
	s_nop 0
	global_load_lds_dwordx4 v[170:171], off
	v_lshl_add_u64 v[170:171], v[216:217], 0, s[26:27]
	s_mov_b32 m0, s76
	s_nop 0
	global_load_lds_dwordx4 v[170:171], off
	v_lshl_add_u64 v[170:171], v[218:219], 0, s[26:27]
	s_mov_b32 m0, s77
	s_nop 0
	global_load_lds_dwordx4 v[170:171], off
	s_waitcnt vmcnt(8)
	s_waitcnt lgkmcnt(0)
	s_barrier
	s_setprio 1
	v_mfma_f32_16x16x32_bf16 v[54:57], v[130:133], v[180:183], v[54:57]
	v_mfma_f32_16x16x32_bf16 v[50:53], v[138:141], v[180:183], v[50:53]
	v_mfma_f32_16x16x32_bf16 v[38:41], v[130:133], v[188:191], v[38:41]
	v_mfma_f32_16x16x32_bf16 v[34:37], v[138:141], v[188:191], v[34:37]
	v_mfma_f32_16x16x32_bf16 v[22:25], v[130:133], v[196:199], v[22:25]
	v_mfma_f32_16x16x32_bf16 v[18:21], v[138:141], v[196:199], v[18:21]
	v_mfma_f32_16x16x32_bf16 v[10:13], v[130:133], v[208:211], v[10:13]
	v_mfma_f32_16x16x32_bf16 v[6:9], v[138:141], v[208:211], v[6:9]
	v_mfma_f32_16x16x32_bf16 v[54:57], v[134:137], v[184:187], v[54:57]
	v_mfma_f32_16x16x32_bf16 v[50:53], v[142:145], v[184:187], v[50:53]
	v_mfma_f32_16x16x32_bf16 v[38:41], v[134:137], v[192:195], v[38:41]
	v_mfma_f32_16x16x32_bf16 v[34:37], v[142:145], v[192:195], v[34:37]
	v_mfma_f32_16x16x32_bf16 v[22:25], v[134:137], v[204:207], v[22:25]
	v_mfma_f32_16x16x32_bf16 v[18:21], v[142:145], v[204:207], v[18:21]
	v_mfma_f32_16x16x32_bf16 v[10:13], v[134:137], v[212:215], v[10:13]
	v_mfma_f32_16x16x32_bf16 v[6:9], v[142:145], v[212:215], v[6:9]
	v_mfma_f32_16x16x32_bf16 v[62:65], v[146:149], v[180:183], v[62:65]
	v_mfma_f32_16x16x32_bf16 v[58:61], v[154:157], v[180:183], v[58:61]
	v_mfma_f32_16x16x32_bf16 v[46:49], v[146:149], v[188:191], v[46:49]
	v_mfma_f32_16x16x32_bf16 v[42:45], v[154:157], v[188:191], v[42:45]
	v_mfma_f32_16x16x32_bf16 v[30:33], v[146:149], v[196:199], v[30:33]
	v_mfma_f32_16x16x32_bf16 v[26:29], v[154:157], v[196:199], v[26:29]
	v_mfma_f32_16x16x32_bf16 v[14:17], v[146:149], v[208:211], v[14:17]
	v_mfma_f32_16x16x32_bf16 v[2:5], v[154:157], v[208:211], v[2:5]
	v_mfma_f32_16x16x32_bf16 v[62:65], v[150:153], v[184:187], v[62:65]
	v_mfma_f32_16x16x32_bf16 v[58:61], v[176:179], v[184:187], v[58:61]
	v_mfma_f32_16x16x32_bf16 v[46:49], v[150:153], v[192:195], v[46:49]
	v_mfma_f32_16x16x32_bf16 v[42:45], v[176:179], v[192:195], v[42:45]
	v_mfma_f32_16x16x32_bf16 v[30:33], v[150:153], v[204:207], v[30:33]
	v_mfma_f32_16x16x32_bf16 v[26:29], v[176:179], v[204:207], v[26:29]
	v_mfma_f32_16x16x32_bf16 v[14:17], v[150:153], v[212:215], v[14:17]
	v_mfma_f32_16x16x32_bf16 v[2:5], v[176:179], v[212:215], v[2:5]
	s_setprio 0
	s_barrier
	s_add_u32 s19, s19, 0x100
	s_addc_u32 s36, s36, 0
	s_add_u32 s37, s37, 0x100
	s_addc_u32 s57, s57, 0
	s_cmp_lt_i32 s56, s18
	s_cbranch_scc1 .LBB0_383

; #define PG8_STAGE(bufoff, gbase, voff) do { _Pragma("unroll") for (int _i = 0; _i < 2; ++_i) \
;         __builtin_amdgcn_global_load_lds((const unsigned*)((const char*)(gbase) + (voff)[_i]), (PG8_LAS unsigned*)(lds + (bufoff) + ldsw + _i * 8192), 16, 0, 0); } while (0)
; #define PG8_LDA(dst, b, h) do { _Pragma("unroll") for (int m = 0; m < 4; ++m) _Pragma("unroll") for (int k = 0; k < 2; ++k) dst[m][k] = *(const PG8_LAS bf16x8*)(lds + PG8_SA(b, h) + aoff + m * 2048 + k * 1024); } while (0)
; #define PG8_LDB(dst, b, h) do { _Pragma("unroll") for (int n = 0; n < 2; ++n) _Pragma("unroll") for (int k = 0; k < 2; ++k) dst[n][k] = *(const PG8_LAS bf16x8*)(lds + PG8_SB(b, h) + boff + n * 2048 + k * 1024); } while (0)
; #define PG8_MMA(ai, bj, At, Bt) do { __builtin_amdgcn_s_setprio(1); _Pragma("unroll") for (int m = 0; m < 4; ++m) _Pragma("unroll") for (int n = 0; n < 2; ++n) _Pragma("unroll") for (int k = 0; k < 2; ++k) \
;         acc[ai][bj][m][n] = __builtin_amdgcn_mfma_f32_16x16x32_bf16(Bt[n][k], At[m][k], acc[ai][bj][m][n], 0, 0, 0); __builtin_amdgcn_s_setprio(0); } while (0)
; #define PG8_WAIT_V(n) asm volatile("s_waitcnt vmcnt(" #n ")" ::: "memory")
; template <class Epi, class Sched, bool ALIGN_EPI = false, bool SP2 = false>
; __device__ __forceinline__ void gemm_phase(PG8_LAS unsigned char* lds, const Gemm g, const Sched& S, const Epi& E) {
;     ...
;             PG8_LDB(B0, 0, 0); PG8_LDB(B1, 0, 1); PG8_SCHED; PG8_LDA(At, 0, 0); PG8_STAGEA(PG8_SA(1, 1), a1, 1, false);
;             PG8_WAIT_V(8); PG8_WAIT_L(0); PG8_BAR; PG8_MMA(0, 0, At, B0); PG8_MMA(0, 1, At, B1); PG8_BAR; PG8_SCHED;
;             PG8_LDA(At, 0, 1); PG8_STAGE(PG8_SB(0, 0), b2, voffB); PG8_STAGE(PG8_SB(0, 1), b2 + hstep, voffB); PG8_STAGEA(PG8_SA(0, 0), a2, 0, last);
;             PG8_WAIT_V(8); PG8_WAIT_L(0); PG8_BAR; PG8_MMA(1, 0, At, B0); PG8_MMA(1, 1, At, B1); PG8_BAR; PG8_SCHED;
;             PG8_LDB(B0, 1, 0); PG8_LDB(B1, 1, 1); PG8_SCHED; PG8_LDA(At, 1, 0); PG8_STAGEA(PG8_SA(0, 1), a2, 1, last);
;             PG8_WAIT_V(8); PG8_WAIT_L(0); PG8_BAR; PG8_MMA(0, 0, At, B0); PG8_MMA(0, 1, At, B1); PG8_BAR; PG8_SCHED;
;             PG8_LDA(At, 1, 1); PG8_STAGE(PG8_SB(1, 0), b3, voffB); PG8_STAGE(PG8_SB(1, 1), b3 + hstep, voffB); PG8_STAGEA(PG8_SA(1, 0), a3, 0, last);
;             PG8_WAIT_V(8); PG8_WAIT_L(0); PG8_BAR; PG8_MMA(1, 0, At, B0); PG8_MMA(1, 1, At, B1); PG8_BAR; PG8_SCHED;
.LBB0_571:
	v_add_u32_e32 v162, s66, v150
	v_add_u32_e32 v178, s67, v150
	ds_read_b128 v[146:149], v162
	ds_read_b128 v[154:157], v162 offset:1024
	ds_read_b128 v[158:161], v162 offset:2048
	ds_read_b128 v[162:165], v162 offset:3072
	ds_read_b128 v[166:169], v178
	ds_read_b128 v[170:173], v178 offset:1024
	ds_read_b128 v[174:177], v178 offset:2048
	ds_read_b128 v[178:181], v178 offset:3072
	s_add_u32 s52, s50, 0xfff80080
	s_addc_u32 s53, s51, -1
	s_cmp_eq_u32 s49, 28
	s_cselect_b32 s55, s9, s53
	s_cselect_b32 s54, s11, s52
	s_cselect_b32 s53, s36, s43
	s_cselect_b32 s52, s37, s41
	v_lshl_add_u64 v[216:217], s[50:51], 0, v[138:139]
	s_add_i32 m0, s57, 0xc000
	ds_read_b128 v[182:185], v152
	ds_read_b128 v[186:189], v152 offset:1024
	ds_read_b128 v[190:193], v152 offset:2048
	ds_read_b128 v[194:197], v152 offset:3072
	ds_read_b128 v[198:201], v152 offset:4096
	ds_read_b128 v[204:207], v152 offset:5120
	ds_read_b128 v[208:211], v152 offset:6144
	ds_read_b128 v[212:215], v152 offset:7168
	global_load_lds_dwordx4 v[216:217], off
	v_lshl_add_u64 v[216:217], s[50:51], 0, v[140:141]
	s_add_i32 m0, s57, 0xe000
	s_nop 0
	global_load_lds_dwordx4 v[216:217], off
	s_waitcnt vmcnt(8)
	s_waitcnt lgkmcnt(0)
	s_barrier
	s_setprio 1
	v_mfma_f32_16x16x32_bf16 v[126:129], v[146:149], v[182:185], v[126:129]
	v_mfma_f32_16x16x32_bf16 v[122:125], v[158:161], v[182:185], v[122:125]
	v_mfma_f32_16x16x32_bf16 v[110:113], v[146:149], v[190:193], v[110:113]
	v_mfma_f32_16x16x32_bf16 v[106:109], v[158:161], v[190:193], v[106:109]
	v_mfma_f32_16x16x32_bf16 v[94:97], v[146:149], v[198:201], v[94:97]
	v_mfma_f32_16x16x32_bf16 v[90:93], v[158:161], v[198:201], v[90:93]
	v_mfma_f32_16x16x32_bf16 v[78:81], v[146:149], v[208:211], v[78:81]
	v_mfma_f32_16x16x32_bf16 v[74:77], v[158:161], v[208:211], v[74:77]
	v_mfma_f32_16x16x32_bf16 v[126:129], v[154:157], v[186:189], v[126:129]
	v_mfma_f32_16x16x32_bf16 v[122:125], v[162:165], v[186:189], v[122:125]
	v_mfma_f32_16x16x32_bf16 v[110:113], v[154:157], v[194:197], v[110:113]
	v_mfma_f32_16x16x32_bf16 v[106:109], v[162:165], v[194:197], v[106:109]
	v_mfma_f32_16x16x32_bf16 v[94:97], v[154:157], v[204:207], v[94:97]
	v_mfma_f32_16x16x32_bf16 v[90:93], v[162:165], v[204:207], v[90:93]
	v_mfma_f32_16x16x32_bf16 v[78:81], v[154:157], v[212:215], v[78:81]
	v_mfma_f32_16x16x32_bf16 v[74:77], v[162:165], v[212:215], v[74:77]
	v_mfma_f32_16x16x32_bf16 v[118:121], v[166:169], v[182:185], v[118:121]
	v_mfma_f32_16x16x32_bf16 v[114:117], v[174:177], v[182:185], v[114:117]
	v_mfma_f32_16x16x32_bf16 v[102:105], v[166:169], v[190:193], v[102:105]
	v_mfma_f32_16x16x32_bf16 v[98:101], v[174:177], v[190:193], v[98:101]
	v_mfma_f32_16x16x32_bf16 v[86:89], v[166:169], v[198:201], v[86:89]
	v_mfma_f32_16x16x32_bf16 v[82:85], v[174:177], v[198:201], v[82:85]
	v_mfma_f32_16x16x32_bf16 v[70:73], v[166:169], v[208:211], v[70:73]
	v_mfma_f32_16x16x32_bf16 v[66:69], v[174:177], v[208:211], v[66:69]
	v_mfma_f32_16x16x32_bf16 v[118:121], v[170:173], v[186:189], v[118:121]
	v_mfma_f32_16x16x32_bf16 v[114:117], v[178:181], v[186:189], v[114:117]
	v_mfma_f32_16x16x32_bf16 v[102:105], v[170:173], v[194:197], v[102:105]
	v_mfma_f32_16x16x32_bf16 v[98:101], v[178:181], v[194:197], v[98:101]
	v_mfma_f32_16x16x32_bf16 v[86:89], v[170:173], v[204:207], v[86:89]
	v_mfma_f32_16x16x32_bf16 v[82:85], v[178:181], v[204:207], v[82:85]
	v_mfma_f32_16x16x32_bf16 v[70:73], v[170:173], v[212:215], v[70:73]
	v_mfma_f32_16x16x32_bf16 v[66:69], v[178:181], v[212:215], v[66:69]
	s_setprio 0
	s_barrier
	s_add_i32 s69, s66, s56
	v_lshl_add_u64 v[216:217], s[52:53], 0, v[132:133]
	s_mov_b32 m0, s69
	ds_read_b128 v[182:185], v152 offset:16384
	ds_read_b128 v[186:189], v152 offset:17408
	ds_read_b128 v[190:193], v152 offset:18432
	ds_read_b128 v[194:197], v152 offset:19456
	ds_read_b128 v[198:201], v152 offset:20480
	ds_read_b128 v[204:207], v152 offset:21504
	ds_read_b128 v[208:211], v152 offset:22528
	ds_read_b128 v[212:215], v152 offset:23552
	global_load_lds_dwordx4 v[216:217], off
	s_add_i32 m0, s69, 0x2000
	s_add_u32 s74, s52, 0x80000
	v_lshl_add_u64 v[218:219], s[52:53], 0, v[136:137]
	s_addc_u32 s75, s53, 0
	s_add_i32 s69, s67, s56
	global_load_lds_dwordx4 v[218:219], off
	v_lshl_add_u64 v[220:221], s[74:75], 0, v[132:133]
	s_mov_b32 m0, s69
	v_lshl_add_u64 v[222:223], s[54:55], 0, v[134:135]
	global_load_lds_dwordx4 v[220:221], off
	v_lshl_add_u64 v[220:221], s[74:75], 0, v[136:137]
	s_add_i32 m0, s69, 0x2000
	s_nop 0
	global_load_lds_dwordx4 v[220:221], off
	v_lshl_add_u64 v[220:221], s[54:55], 0, v[130:131]
	s_mov_b32 m0, s57
	s_nop 0
	global_load_lds_dwordx4 v[220:221], off
	s_mov_b32 m0, s58
	s_nop 0
	global_load_lds_dwordx4 v[222:223], off
	s_waitcnt vmcnt(8)
	s_waitcnt lgkmcnt(0)
	s_barrier
; #define PG8_STAGE(bufoff, gbase, voff) do { _Pragma("unroll") for (int _i = 0; _i < 2; ++_i) \
;         __builtin_amdgcn_global_load_lds((const unsigned*)((const char*)(gbase) + (voff)[_i]), (PG8_LAS unsigned*)(lds + (bufoff) + ldsw + _i * 8192), 16, 0, 0); } while (0)
; #define PG8_LDA(dst, b, h) do { _Pragma("unroll") for (int m = 0; m < 4; ++m) _Pragma("unroll") for (int k = 0; k < 2; ++k) dst[m][k] = *(const PG8_LAS bf16x8*)(lds + PG8_SA(b, h) + aoff + m * 2048 + k * 1024); } while (0)
; #define PG8_LDB(dst, b, h) do { _Pragma("unroll") for (int n = 0; n < 2; ++n) _Pragma("unroll") for (int k = 0; k < 2; ++k) dst[n][k] = *(const PG8_LAS bf16x8*)(lds + PG8_SB(b, h) + boff + n * 2048 + k * 1024); } while (0)
; #define PG8_MMA(ai, bj, At, Bt) do { __builtin_amdgcn_s_setprio(1); _Pragma("unroll") for (int m = 0; m < 4; ++m) _Pragma("unroll") for (int n = 0; n < 2; ++n) _Pragma("unroll") for (int k = 0; k < 2; ++k) \
;         acc[ai][bj][m][n] = __builtin_amdgcn_mfma_f32_16x16x32_bf16(Bt[n][k], At[m][k], acc[ai][bj][m][n], 0, 0, 0); __builtin_amdgcn_s_setprio(0); } while (0)
; #define PG8_WAIT_V(n) asm volatile("s_waitcnt vmcnt(" #n ")" ::: "memory")
; #define PG8_WAIT_L(n) asm volatile("s_waitcnt lgkmcnt(" #n ")" ::: "memory")
; #define PG8_BAR __builtin_amdgcn_s_barrier()
; #define PG8_SCHED __builtin_amdgcn_sched_barrier(0)
; template <class Epi, class Sched, bool ALIGN_EPI = false, bool SP2 = false>
; __device__ __forceinline__ void gemm_phase(PG8_LAS unsigned char* lds, const Gemm g, const Sched& S, const Epi& E) {
;     ...
;             PG8_LDA(At, 0, 1); PG8_STAGE(PG8_SB(0, 0), b2, voffB); PG8_STAGE(PG8_SB(0, 1), b2 + hstep, voffB); PG8_STAGEA(PG8_SA(0, 0), a2, 0, last);
;             PG8_WAIT_V(8); PG8_WAIT_L(0); PG8_BAR; PG8_MMA(1, 0, At, B0); PG8_MMA(1, 1, At, B1); PG8_BAR; PG8_SCHED;
;             PG8_LDB(B0, 1, 0); PG8_LDB(B1, 1, 1); PG8_SCHED; PG8_LDA(At, 1, 0); PG8_STAGEA(PG8_SA(0, 1), a2, 1, last);
;             PG8_WAIT_V(8); PG8_WAIT_L(0); PG8_BAR; PG8_MMA(0, 0, At, B0); PG8_MMA(0, 1, At, B1); PG8_BAR; PG8_SCHED;
	s_setprio 1
	v_mfma_f32_16x16x32_bf16 v[62:65], v[146:149], v[182:185], v[62:65]
	v_mfma_f32_16x16x32_bf16 v[58:61], v[158:161], v[182:185], v[58:61]
	v_mfma_f32_16x16x32_bf16 v[46:49], v[146:149], v[190:193], v[46:49]
	v_mfma_f32_16x16x32_bf16 v[42:45], v[158:161], v[190:193], v[42:45]
	v_mfma_f32_16x16x32_bf16 v[30:33], v[146:149], v[198:201], v[30:33]
	v_mfma_f32_16x16x32_bf16 v[26:29], v[158:161], v[198:201], v[26:29]
	v_mfma_f32_16x16x32_bf16 v[14:17], v[146:149], v[208:211], v[14:17]
	v_mfma_f32_16x16x32_bf16 v[10:13], v[158:161], v[208:211], v[10:13]
	v_mfma_f32_16x16x32_bf16 v[62:65], v[154:157], v[186:189], v[62:65]
	v_mfma_f32_16x16x32_bf16 v[58:61], v[162:165], v[186:189], v[58:61]
	v_mfma_f32_16x16x32_bf16 v[46:49], v[154:157], v[194:197], v[46:49]
	v_mfma_f32_16x16x32_bf16 v[42:45], v[162:165], v[194:197], v[42:45]
	v_mfma_f32_16x16x32_bf16 v[30:33], v[154:157], v[204:207], v[30:33]
	v_mfma_f32_16x16x32_bf16 v[26:29], v[162:165], v[204:207], v[26:29]
	v_mfma_f32_16x16x32_bf16 v[14:17], v[154:157], v[212:215], v[14:17]
	v_mfma_f32_16x16x32_bf16 v[10:13], v[162:165], v[212:215], v[10:13]
	v_mfma_f32_16x16x32_bf16 v[54:57], v[166:169], v[182:185], v[54:57]
	v_mfma_f32_16x16x32_bf16 v[50:53], v[174:177], v[182:185], v[50:53]
	v_mfma_f32_16x16x32_bf16 v[38:41], v[166:169], v[190:193], v[38:41]
	v_mfma_f32_16x16x32_bf16 v[34:37], v[174:177], v[190:193], v[34:37]
	v_mfma_f32_16x16x32_bf16 v[22:25], v[166:169], v[198:201], v[22:25]
	v_mfma_f32_16x16x32_bf16 v[18:21], v[174:177], v[198:201], v[18:21]
	v_mfma_f32_16x16x32_bf16 v[6:9], v[166:169], v[208:211], v[6:9]
	v_mfma_f32_16x16x32_bf16 v[2:5], v[174:177], v[208:211], v[2:5]
	v_mfma_f32_16x16x32_bf16 v[54:57], v[170:173], v[186:189], v[54:57]
	v_mfma_f32_16x16x32_bf16 v[50:53], v[178:181], v[186:189], v[50:53]
	v_mfma_f32_16x16x32_bf16 v[38:41], v[170:173], v[194:197], v[38:41]
	v_mfma_f32_16x16x32_bf16 v[34:37], v[178:181], v[194:197], v[34:37]
	v_mfma_f32_16x16x32_bf16 v[22:25], v[170:173], v[204:207], v[22:25]
	v_mfma_f32_16x16x32_bf16 v[18:21], v[178:181], v[204:207], v[18:21]
	v_mfma_f32_16x16x32_bf16 v[6:9], v[170:173], v[212:215], v[6:9]
	v_mfma_f32_16x16x32_bf16 v[2:5], v[178:181], v[212:215], v[2:5]
	s_setprio 0
	s_barrier
	s_add_i32 s69, 0, 0x18000
	s_add_i32 s74, 0, 0x1c000
	v_add_u32_e32 v162, s69, v150
	v_add_u32_e32 v178, s74, v150
	ds_read_b128 v[146:149], v162
	ds_read_b128 v[154:157], v162 offset:1024
	ds_read_b128 v[158:161], v162 offset:2048
	ds_read_b128 v[162:165], v162 offset:3072
	ds_read_b128 v[166:169], v178
	ds_read_b128 v[170:173], v178 offset:1024
	ds_read_b128 v[174:177], v178 offset:2048
	ds_read_b128 v[178:181], v178 offset:3072
	s_add_u32 s54, s54, 0x80000
	s_addc_u32 s55, s55, 0
	s_mov_b32 m0, s59
	v_lshl_add_u64 v[224:225], s[54:55], 0, v[130:131]
	ds_read_b128 v[182:185], v152 offset:32768
	ds_read_b128 v[186:189], v152 offset:33792
	ds_read_b128 v[190:193], v152 offset:34816
	ds_read_b128 v[194:197], v152 offset:35840
	ds_read_b128 v[198:201], v152 offset:36864
	ds_read_b128 v[204:207], v152 offset:37888
	ds_read_b128 v[208:211], v152 offset:38912
	ds_read_b128 v[212:215], v152 offset:39936
	global_load_lds_dwordx4 v[224:225], off
	v_lshl_add_u64 v[224:225], s[54:55], 0, v[134:135]
	s_mov_b32 m0, s60
	s_nop 0
	global_load_lds_dwordx4 v[224:225], off
	s_waitcnt vmcnt(8)
	s_waitcnt lgkmcnt(0)
	s_barrier
	s_setprio 1
	v_mfma_f32_16x16x32_bf16 v[126:129], v[146:149], v[182:185], v[126:129]
	v_mfma_f32_16x16x32_bf16 v[122:125], v[158:161], v[182:185], v[122:125]
	v_mfma_f32_16x16x32_bf16 v[110:113], v[146:149], v[190:193], v[110:113]
	v_mfma_f32_16x16x32_bf16 v[106:109], v[158:161], v[190:193], v[106:109]
	v_mfma_f32_16x16x32_bf16 v[94:97], v[146:149], v[198:201], v[94:97]
	v_mfma_f32_16x16x32_bf16 v[90:93], v[158:161], v[198:201], v[90:93]
	v_mfma_f32_16x16x32_bf16 v[78:81], v[146:149], v[208:211], v[78:81]
	v_mfma_f32_16x16x32_bf16 v[74:77], v[158:161], v[208:211], v[74:77]
	v_mfma_f32_16x16x32_bf16 v[126:129], v[154:157], v[186:189], v[126:129]
	v_mfma_f32_16x16x32_bf16 v[122:125], v[162:165], v[186:189], v[122:125]
	v_mfma_f32_16x16x32_bf16 v[110:113], v[154:157], v[194:197], v[110:113]
	v_mfma_f32_16x16x32_bf16 v[106:109], v[162:165], v[194:197], v[106:109]
	v_mfma_f32_16x16x32_bf16 v[94:97], v[154:157], v[204:207], v[94:97]
	v_mfma_f32_16x16x32_bf16 v[90:93], v[162:165], v[204:207], v[90:93]
	v_mfma_f32_16x16x32_bf16 v[78:81], v[154:157], v[212:215], v[78:81]
	v_mfma_f32_16x16x32_bf16 v[74:77], v[162:165], v[212:215], v[74:77]
	v_mfma_f32_16x16x32_bf16 v[118:121], v[166:169], v[182:185], v[118:121]
	v_mfma_f32_16x16x32_bf16 v[114:117], v[174:177], v[182:185], v[114:117]
	v_mfma_f32_16x16x32_bf16 v[102:105], v[166:169], v[190:193], v[102:105]
	v_mfma_f32_16x16x32_bf16 v[98:101], v[174:177], v[190:193], v[98:101]
	v_mfma_f32_16x16x32_bf16 v[86:89], v[166:169], v[198:201], v[86:89]
	v_mfma_f32_16x16x32_bf16 v[82:85], v[174:177], v[198:201], v[82:85]
	v_mfma_f32_16x16x32_bf16 v[70:73], v[166:169], v[208:211], v[70:73]
	v_mfma_f32_16x16x32_bf16 v[66:69], v[174:177], v[208:211], v[66:69]
	v_mfma_f32_16x16x32_bf16 v[118:121], v[170:173], v[186:189], v[118:121]
	v_mfma_f32_16x16x32_bf16 v[114:117], v[178:181], v[186:189], v[114:117]
	v_mfma_f32_16x16x32_bf16 v[102:105], v[170:173], v[194:197], v[102:105]
	v_mfma_f32_16x16x32_bf16 v[98:101], v[178:181], v[194:197], v[98:101]
	v_mfma_f32_16x16x32_bf16 v[86:89], v[170:173], v[204:207], v[86:89]
	v_mfma_f32_16x16x32_bf16 v[82:85], v[178:181], v[204:207], v[82:85]
	v_mfma_f32_16x16x32_bf16 v[70:73], v[170:173], v[212:215], v[70:73]
	v_mfma_f32_16x16x32_bf16 v[66:69], v[178:181], v[212:215], v[66:69]
	s_setprio 0
	s_barrier
; #define PG8_STAGE(bufoff, gbase, voff) do { _Pragma("unroll") for (int _i = 0; _i < 2; ++_i) \
;         __builtin_amdgcn_global_load_lds((const unsigned*)((const char*)(gbase) + (voff)[_i]), (PG8_LAS unsigned*)(lds + (bufoff) + ldsw + _i * 8192), 16, 0, 0); } while (0)
; #define PG8_LDA(dst, b, h) do { _Pragma("unroll") for (int m = 0; m < 4; ++m) _Pragma("unroll") for (int k = 0; k < 2; ++k) dst[m][k] = *(const PG8_LAS bf16x8*)(lds + PG8_SA(b, h) + aoff + m * 2048 + k * 1024); } while (0)
; #define PG8_MMA(ai, bj, At, Bt) do { __builtin_amdgcn_s_setprio(1); _Pragma("unroll") for (int m = 0; m < 4; ++m) _Pragma("unroll") for (int n = 0; n < 2; ++n) _Pragma("unroll") for (int k = 0; k < 2; ++k) \
;         acc[ai][bj][m][n] = __builtin_amdgcn_mfma_f32_16x16x32_bf16(Bt[n][k], At[m][k], acc[ai][bj][m][n], 0, 0, 0); __builtin_amdgcn_s_setprio(0); } while (0)
; #define PG8_WAIT_V(n) asm volatile("s_waitcnt vmcnt(" #n ")" ::: "memory")
; #define PG8_WAIT_L(n) asm volatile("s_waitcnt lgkmcnt(" #n ")" ::: "memory")
; #define PG8_BAR __builtin_amdgcn_s_barrier()
; #define PG8_SCHED __builtin_amdgcn_sched_barrier(0)
; template <class Epi, class Sched, bool ALIGN_EPI = false, bool SP2 = false>
; __device__ __forceinline__ void gemm_phase(PG8_LAS unsigned char* lds, const Gemm g, const Sched& S, const Epi& E) {
;     ...
;         for (; t < tend; t += 2) {
;             const bool last = (t == nt - 2);
;             const char* a1 = cA + (size_t)(t + 1) * kstep;
;             const char* a2 = last ? nA : cA + (size_t)(t + 2) * kstep; const char* b2 = last ? nB : cB + (size_t)(t + 2) * kstep;
;     ...
;             PG8_LDA(At, 1, 1); PG8_STAGE(PG8_SB(1, 0), b3, voffB); PG8_STAGE(PG8_SB(1, 1), b3 + hstep, voffB); PG8_STAGEA(PG8_SA(1, 0), a3, 0, last);
;             PG8_WAIT_V(8); PG8_WAIT_L(0); PG8_BAR; PG8_MMA(1, 0, At, B0); PG8_MMA(1, 1, At, B1); PG8_BAR; PG8_SCHED;
	s_add_i32 s54, s69, s56
	v_lshl_add_u64 v[216:217], v[216:217], 0, s[26:27]
	s_mov_b32 m0, s54
	ds_read_b128 v[182:185], v152 offset:49152
	ds_read_b128 v[186:189], v152 offset:50176
	ds_read_b128 v[190:193], v152 offset:51200
	ds_read_b128 v[194:197], v152 offset:52224
	ds_read_b128 v[198:201], v152 offset:53248
	ds_read_b128 v[204:207], v152 offset:54272
	ds_read_b128 v[208:211], v152 offset:55296
	ds_read_b128 v[212:215], v152 offset:56320
	global_load_lds_dwordx4 v[216:217], off
	s_add_i32 m0, s54, 0x2000
	s_add_u32 s52, s52, 0x80080
	v_lshl_add_u64 v[216:217], v[218:219], 0, s[26:27]
	s_addc_u32 s53, s53, 0
	s_add_i32 s54, s74, s56
	global_load_lds_dwordx4 v[216:217], off
	v_lshl_add_u64 v[216:217], s[52:53], 0, v[132:133]
	s_mov_b32 m0, s54
	s_nop 0
	global_load_lds_dwordx4 v[216:217], off
	v_lshl_add_u64 v[216:217], s[52:53], 0, v[136:137]
	s_add_i32 m0, s54, 0x2000
	s_nop 0
	global_load_lds_dwordx4 v[216:217], off
	v_lshl_add_u64 v[216:217], v[220:221], 0, s[26:27]
	s_mov_b32 m0, s62
	s_nop 0
	global_load_lds_dwordx4 v[216:217], off
	v_lshl_add_u64 v[216:217], v[222:223], 0, s[26:27]
	s_mov_b32 m0, s63
	s_nop 0
	global_load_lds_dwordx4 v[216:217], off
	s_waitcnt vmcnt(8)
	s_waitcnt lgkmcnt(0)
	s_barrier
	s_setprio 1
	v_mfma_f32_16x16x32_bf16 v[62:65], v[146:149], v[182:185], v[62:65]
	v_mfma_f32_16x16x32_bf16 v[58:61], v[158:161], v[182:185], v[58:61]
	v_mfma_f32_16x16x32_bf16 v[46:49], v[146:149], v[190:193], v[46:49]
	v_mfma_f32_16x16x32_bf16 v[42:45], v[158:161], v[190:193], v[42:45]
	v_mfma_f32_16x16x32_bf16 v[30:33], v[146:149], v[198:201], v[30:33]
	v_mfma_f32_16x16x32_bf16 v[26:29], v[158:161], v[198:201], v[26:29]
	v_mfma_f32_16x16x32_bf16 v[14:17], v[146:149], v[208:211], v[14:17]
	v_mfma_f32_16x16x32_bf16 v[10:13], v[158:161], v[208:211], v[10:13]
	v_mfma_f32_16x16x32_bf16 v[62:65], v[154:157], v[186:189], v[62:65]
	v_mfma_f32_16x16x32_bf16 v[58:61], v[162:165], v[186:189], v[58:61]
	v_mfma_f32_16x16x32_bf16 v[46:49], v[154:157], v[194:197], v[46:49]
	v_mfma_f32_16x16x32_bf16 v[42:45], v[162:165], v[194:197], v[42:45]
	v_mfma_f32_16x16x32_bf16 v[30:33], v[154:157], v[204:207], v[30:33]
	v_mfma_f32_16x16x32_bf16 v[26:29], v[162:165], v[204:207], v[26:29]
	v_mfma_f32_16x16x32_bf16 v[14:17], v[154:157], v[212:215], v[14:17]
	v_mfma_f32_16x16x32_bf16 v[10:13], v[162:165], v[212:215], v[10:13]
	v_mfma_f32_16x16x32_bf16 v[54:57], v[166:169], v[182:185], v[54:57]
	v_mfma_f32_16x16x32_bf16 v[50:53], v[174:177], v[182:185], v[50:53]
	v_mfma_f32_16x16x32_bf16 v[38:41], v[166:169], v[190:193], v[38:41]
	v_mfma_f32_16x16x32_bf16 v[34:37], v[174:177], v[190:193], v[34:37]
	v_mfma_f32_16x16x32_bf16 v[22:25], v[166:169], v[198:201], v[22:25]
	v_mfma_f32_16x16x32_bf16 v[18:21], v[174:177], v[198:201], v[18:21]
	v_mfma_f32_16x16x32_bf16 v[6:9], v[166:169], v[208:211], v[6:9]
	v_mfma_f32_16x16x32_bf16 v[2:5], v[174:177], v[208:211], v[2:5]
	v_mfma_f32_16x16x32_bf16 v[54:57], v[170:173], v[186:189], v[54:57]
	v_mfma_f32_16x16x32_bf16 v[50:53], v[178:181], v[186:189], v[50:53]
	v_mfma_f32_16x16x32_bf16 v[38:41], v[170:173], v[194:197], v[38:41]
	v_mfma_f32_16x16x32_bf16 v[34:37], v[178:181], v[194:197], v[34:37]
	v_mfma_f32_16x16x32_bf16 v[22:25], v[170:173], v[204:207], v[22:25]
	v_mfma_f32_16x16x32_bf16 v[18:21], v[178:181], v[204:207], v[18:21]
	v_mfma_f32_16x16x32_bf16 v[6:9], v[170:173], v[212:215], v[6:9]
	v_mfma_f32_16x16x32_bf16 v[2:5], v[178:181], v[212:215], v[2:5]
	s_setprio 0
	s_barrier
	s_add_i32 s49, s49, 2
	s_add_u32 s50, s50, 0x100
	s_addc_u32 s51, s51, 0
	s_add_u32 s41, s41, 0x100
	s_addc_u32 s43, s43, 0
	s_cmp_gt_u32 s49, 29
	s_cbranch_scc0 .LBB0_571
	s_and_b64 vcc, exec, s[38:39]
	s_cbranch_vccz .LBB0_574
	s_barrier

; #define PG8_STAGE(bufoff, gbase, voff) do { _Pragma("unroll") for (int _i = 0; _i < 2; ++_i) \
;         __builtin_amdgcn_global_load_lds((const unsigned*)((const char*)(gbase) + (voff)[_i]), (PG8_LAS unsigned*)(lds + (bufoff) + ldsw + _i * 8192), 16, 0, 0); } while (0)
; #define PG8_LDA(dst, b, h) do { _Pragma("unroll") for (int m = 0; m < 4; ++m) _Pragma("unroll") for (int k = 0; k < 2; ++k) dst[m][k] = *(const PG8_LAS bf16x8*)(lds + PG8_SA(b, h) + aoff + m * 2048 + k * 1024); } while (0)
; #define PG8_LDB(dst, b, h) do { _Pragma("unroll") for (int n = 0; n < 2; ++n) _Pragma("unroll") for (int k = 0; k < 2; ++k) dst[n][k] = *(const PG8_LAS bf16x8*)(lds + PG8_SB(b, h) + boff + n * 2048 + k * 1024); } while (0)
; #define PG8_MMA(ai, bj, At, Bt) do { __builtin_amdgcn_s_setprio(1); _Pragma("unroll") for (int m = 0; m < 4; ++m) _Pragma("unroll") for (int n = 0; n < 2; ++n) _Pragma("unroll") for (int k = 0; k < 2; ++k) \
;         acc[ai][bj][m][n] = __builtin_amdgcn_mfma_f32_16x16x32_bf16(Bt[n][k], At[m][k], acc[ai][bj][m][n], 0, 0, 0); __builtin_amdgcn_s_setprio(0); } while (0)
; #define PG8_WAIT_V(n) asm volatile("s_waitcnt vmcnt(" #n ")" ::: "memory")
; #define PG8_WAIT_L(n) asm volatile("s_waitcnt lgkmcnt(" #n ")" ::: "memory")
; #define PG8_BAR __builtin_amdgcn_s_barrier()
; #define PG8_SCHED __builtin_amdgcn_sched_barrier(0)
; template <class Epi, class Sched, bool ALIGN_EPI = false, bool SP2 = false>
; __device__ __forceinline__ void gemm_phase(PG8_LAS unsigned char* lds, const Gemm g, const Sched& S, const Epi& E) {
;     ...
;             PG8_LDB(B0, 0, 0); PG8_LDB(B1, 0, 1); PG8_SCHED; PG8_LDA(At, 0, 0); PG8_STAGEA(PG8_SA(1, 1), a1, 1, false);
;             PG8_WAIT_V(8); PG8_WAIT_L(0); PG8_BAR; PG8_MMA(0, 0, At, B0); PG8_MMA(0, 1, At, B1); PG8_BAR; PG8_SCHED;
;             PG8_LDA(At, 0, 1); PG8_STAGE(PG8_SB(0, 0), b2, voffB); PG8_STAGE(PG8_SB(0, 1), b2 + hstep, voffB); PG8_STAGEA(PG8_SA(0, 0), a2, 0, last);
;             PG8_WAIT_V(8); PG8_WAIT_L(0); PG8_BAR; PG8_MMA(1, 0, At, B0); PG8_MMA(1, 1, At, B1); PG8_BAR; PG8_SCHED;
.LBB0_792:
	s_add_u32 s6, s12, 0x100
	v_add_u32_e32 v134, s84, v152
	s_addc_u32 s7, s13, 0
	ds_read_b128 v[162:165], v134
	ds_read_b128 v[166:169], v134 offset:1024
	ds_read_b128 v[170:173], v134 offset:2048
	ds_read_b128 v[174:177], v134 offset:3072
	v_add_u32_e32 v134, s85, v152
	s_add_u32 s10, s16, s12
	ds_read_b128 v[178:181], v134
	ds_read_b128 v[182:185], v134 offset:1024
	ds_read_b128 v[186:189], v134 offset:2048
	ds_read_b128 v[190:193], v134 offset:3072
	s_addc_u32 s11, s17, s13
	s_cmpk_eq_i32 s12, 0xf00
	s_cselect_b64 vcc, -1, 0
	s_and_b64 s[8:9], vcc, exec
	s_cselect_b32 s36, 0, s6
	s_cselect_b32 s27, 0, s7
	s_cselect_b32 s8, s18, s10
	s_cselect_b32 s9, s15, s11
	s_add_u32 s10, s42, s36
	s_addc_u32 s11, s43, s27
	v_lshl_add_u64 v[228:229], v[142:143], 0, s[12:13]
	s_add_i32 m0, s77, 0xc000
	ds_read_b128 v[194:197], v156
	ds_read_b128 v[198:201], v156 offset:1024
	ds_read_b128 v[204:207], v156 offset:2048
	ds_read_b128 v[208:211], v156 offset:3072
	ds_read_b128 v[212:215], v156 offset:4096
	ds_read_b128 v[216:219], v156 offset:5120
	ds_read_b128 v[220:223], v156 offset:6144
	ds_read_b128 v[224:227], v156 offset:7168
	global_load_lds_dwordx4 v[228:229], off
	v_lshl_add_u64 v[228:229], v[144:145], 0, s[12:13]
	s_add_i32 m0, s77, 0xe000
	s_nop 0
	global_load_lds_dwordx4 v[228:229], off
	s_waitcnt vmcnt(8)
	s_waitcnt lgkmcnt(0)
	s_barrier
	s_setprio 1
	v_mfma_f32_16x16x32_bf16 v[126:129], v[162:165], v[194:197], v[126:129]
	v_mfma_f32_16x16x32_bf16 v[118:121], v[170:173], v[194:197], v[118:121]
	v_mfma_f32_16x16x32_bf16 v[110:113], v[162:165], v[204:207], v[110:113]
	v_mfma_f32_16x16x32_bf16 v[102:105], v[170:173], v[204:207], v[102:105]
	v_mfma_f32_16x16x32_bf16 v[94:97], v[162:165], v[212:215], v[94:97]
	v_mfma_f32_16x16x32_bf16 v[86:89], v[170:173], v[212:215], v[86:89]
	v_mfma_f32_16x16x32_bf16 v[78:81], v[162:165], v[220:223], v[78:81]
	v_mfma_f32_16x16x32_bf16 v[70:73], v[170:173], v[220:223], v[70:73]
	v_mfma_f32_16x16x32_bf16 v[126:129], v[166:169], v[198:201], v[126:129]
	v_mfma_f32_16x16x32_bf16 v[118:121], v[174:177], v[198:201], v[118:121]
	v_mfma_f32_16x16x32_bf16 v[110:113], v[166:169], v[208:211], v[110:113]
	v_mfma_f32_16x16x32_bf16 v[102:105], v[174:177], v[208:211], v[102:105]
	v_mfma_f32_16x16x32_bf16 v[94:97], v[166:169], v[216:219], v[94:97]
	v_mfma_f32_16x16x32_bf16 v[86:89], v[174:177], v[216:219], v[86:89]
	v_mfma_f32_16x16x32_bf16 v[78:81], v[166:169], v[224:227], v[78:81]
	v_mfma_f32_16x16x32_bf16 v[70:73], v[174:177], v[224:227], v[70:73]
	v_mfma_f32_16x16x32_bf16 v[122:125], v[178:181], v[194:197], v[122:125]
	v_mfma_f32_16x16x32_bf16 v[114:117], v[186:189], v[194:197], v[114:117]
	v_mfma_f32_16x16x32_bf16 v[106:109], v[178:181], v[204:207], v[106:109]
	v_mfma_f32_16x16x32_bf16 v[98:101], v[186:189], v[204:207], v[98:101]
	v_mfma_f32_16x16x32_bf16 v[90:93], v[178:181], v[212:215], v[90:93]
	v_mfma_f32_16x16x32_bf16 v[82:85], v[186:189], v[212:215], v[82:85]
	v_mfma_f32_16x16x32_bf16 v[74:77], v[178:181], v[220:223], v[74:77]
	v_mfma_f32_16x16x32_bf16 v[66:69], v[186:189], v[220:223], v[66:69]
	v_mfma_f32_16x16x32_bf16 v[122:125], v[182:185], v[198:201], v[122:125]
	v_mfma_f32_16x16x32_bf16 v[114:117], v[190:193], v[198:201], v[114:117]
	v_mfma_f32_16x16x32_bf16 v[106:109], v[182:185], v[208:211], v[106:109]
	v_mfma_f32_16x16x32_bf16 v[98:101], v[190:193], v[208:211], v[98:101]
	v_mfma_f32_16x16x32_bf16 v[90:93], v[182:185], v[216:219], v[90:93]
	v_mfma_f32_16x16x32_bf16 v[82:85], v[190:193], v[216:219], v[82:85]
	v_mfma_f32_16x16x32_bf16 v[74:77], v[182:185], v[224:227], v[74:77]
	v_mfma_f32_16x16x32_bf16 v[66:69], v[190:193], v[224:227], v[66:69]
	s_setprio 0
	s_barrier
	s_add_i32 s12, s84, s76
	v_lshl_add_u64 v[228:229], s[8:9], 0, v[130:131]
	s_mov_b32 m0, s12
	ds_read_b128 v[194:197], v156 offset:16384
	ds_read_b128 v[198:201], v156 offset:17408
	ds_read_b128 v[204:207], v156 offset:18432
	ds_read_b128 v[208:211], v156 offset:19456
	ds_read_b128 v[212:215], v156 offset:20480
	ds_read_b128 v[216:219], v156 offset:21504
	ds_read_b128 v[220:223], v156 offset:22528
	ds_read_b128 v[224:227], v156 offset:23552
	global_load_lds_dwordx4 v[228:229], off
	s_add_i32 m0, s12, 0x2000
	s_add_u32 s12, s8, 0x80000
	v_lshl_add_u64 v[230:231], s[8:9], 0, v[132:133]
	s_addc_u32 s13, s9, 0
	s_add_i32 s27, s85, s76
	global_load_lds_dwordx4 v[230:231], off
	v_lshl_add_u64 v[232:233], s[12:13], 0, v[130:131]
	s_mov_b32 m0, s27
	v_cndmask_b32_e32 v134, v146, v157, vcc
	global_load_lds_dwordx4 v[232:233], off
	v_lshl_add_u64 v[232:233], s[12:13], 0, v[132:133]
	s_add_i32 m0, s27, 0x2000
	s_nop 0
	global_load_lds_dwordx4 v[232:233], off
	s_mov_b32 m0, s77
	v_lshl_add_u64 v[232:233], s[10:11], 0, v[134:135]
	global_load_lds_dwordx4 v134, s[10:11]
	v_cndmask_b32_e32 v134, v136, v158, vcc
	s_mov_b32 m0, s78
	v_lshl_add_u64 v[234:235], s[10:11], 0, v[134:135]
	global_load_lds_dwordx4 v134, s[10:11]
	s_waitcnt vmcnt(8)
	s_waitcnt lgkmcnt(0)
	s_barrier
; #define PG8_LDA(dst, b, h) do { _Pragma("unroll") for (int m = 0; m < 4; ++m) _Pragma("unroll") for (int k = 0; k < 2; ++k) dst[m][k] = *(const PG8_LAS bf16x8*)(lds + PG8_SA(b, h) + aoff + m * 2048 + k * 1024); } while (0)
; #define PG8_LDB(dst, b, h) do { _Pragma("unroll") for (int n = 0; n < 2; ++n) _Pragma("unroll") for (int k = 0; k < 2; ++k) dst[n][k] = *(const PG8_LAS bf16x8*)(lds + PG8_SB(b, h) + boff + n * 2048 + k * 1024); } while (0)
; #define PG8_MMA(ai, bj, At, Bt) do { __builtin_amdgcn_s_setprio(1); _Pragma("unroll") for (int m = 0; m < 4; ++m) _Pragma("unroll") for (int n = 0; n < 2; ++n) _Pragma("unroll") for (int k = 0; k < 2; ++k) \
;         acc[ai][bj][m][n] = __builtin_amdgcn_mfma_f32_16x16x32_bf16(Bt[n][k], At[m][k], acc[ai][bj][m][n], 0, 0, 0); __builtin_amdgcn_s_setprio(0); } while (0)
; #define PG8_WAIT_V(n) asm volatile("s_waitcnt vmcnt(" #n ")" ::: "memory")
; #define PG8_WAIT_L(n) asm volatile("s_waitcnt lgkmcnt(" #n ")" ::: "memory")
; #define PG8_BAR __builtin_amdgcn_s_barrier()
; #define PG8_SCHED __builtin_amdgcn_sched_barrier(0)
; template <class Epi, class Sched, bool ALIGN_EPI = false, bool SP2 = false>
; __device__ __forceinline__ void gemm_phase(PG8_LAS unsigned char* lds, const Gemm g, const Sched& S, const Epi& E) {
;     ...
;             PG8_WAIT_V(8); PG8_WAIT_L(0); PG8_BAR; PG8_MMA(1, 0, At, B0); PG8_MMA(1, 1, At, B1); PG8_BAR; PG8_SCHED;
;             PG8_LDB(B0, 1, 0); PG8_LDB(B1, 1, 1); PG8_SCHED; PG8_LDA(At, 1, 0); PG8_STAGEA(PG8_SA(0, 1), a2, 1, last);
;             PG8_WAIT_V(8); PG8_WAIT_L(0); PG8_BAR; PG8_MMA(0, 0, At, B0); PG8_MMA(0, 1, At, B1); PG8_BAR; PG8_SCHED;
	s_setprio 1
	v_mfma_f32_16x16x32_bf16 v[62:65], v[162:165], v[194:197], v[62:65]
	v_mfma_f32_16x16x32_bf16 v[54:57], v[170:173], v[194:197], v[54:57]
	v_mfma_f32_16x16x32_bf16 v[46:49], v[162:165], v[204:207], v[46:49]
	v_mfma_f32_16x16x32_bf16 v[38:41], v[170:173], v[204:207], v[38:41]
	v_mfma_f32_16x16x32_bf16 v[30:33], v[162:165], v[212:215], v[30:33]
	v_mfma_f32_16x16x32_bf16 v[22:25], v[170:173], v[212:215], v[22:25]
	v_mfma_f32_16x16x32_bf16 v[14:17], v[162:165], v[220:223], v[14:17]
	v_mfma_f32_16x16x32_bf16 v[6:9], v[170:173], v[220:223], v[6:9]
	v_mfma_f32_16x16x32_bf16 v[62:65], v[166:169], v[198:201], v[62:65]
	v_mfma_f32_16x16x32_bf16 v[54:57], v[174:177], v[198:201], v[54:57]
	v_mfma_f32_16x16x32_bf16 v[46:49], v[166:169], v[208:211], v[46:49]
	v_mfma_f32_16x16x32_bf16 v[38:41], v[174:177], v[208:211], v[38:41]
	v_mfma_f32_16x16x32_bf16 v[30:33], v[166:169], v[216:219], v[30:33]
	v_mfma_f32_16x16x32_bf16 v[22:25], v[174:177], v[216:219], v[22:25]
	v_mfma_f32_16x16x32_bf16 v[14:17], v[166:169], v[224:227], v[14:17]
	v_mfma_f32_16x16x32_bf16 v[6:9], v[174:177], v[224:227], v[6:9]
	v_mfma_f32_16x16x32_bf16 v[58:61], v[178:181], v[194:197], v[58:61]
	v_mfma_f32_16x16x32_bf16 v[50:53], v[186:189], v[194:197], v[50:53]
	v_mfma_f32_16x16x32_bf16 v[42:45], v[178:181], v[204:207], v[42:45]
	v_mfma_f32_16x16x32_bf16 v[34:37], v[186:189], v[204:207], v[34:37]
	v_mfma_f32_16x16x32_bf16 v[26:29], v[178:181], v[212:215], v[26:29]
	v_mfma_f32_16x16x32_bf16 v[18:21], v[186:189], v[212:215], v[18:21]
	v_mfma_f32_16x16x32_bf16 v[10:13], v[178:181], v[220:223], v[10:13]
	v_mfma_f32_16x16x32_bf16 v[2:5], v[186:189], v[220:223], v[2:5]
	v_mfma_f32_16x16x32_bf16 v[58:61], v[182:185], v[198:201], v[58:61]
	v_mfma_f32_16x16x32_bf16 v[50:53], v[190:193], v[198:201], v[50:53]
	v_mfma_f32_16x16x32_bf16 v[42:45], v[182:185], v[208:211], v[42:45]
	v_mfma_f32_16x16x32_bf16 v[34:37], v[190:193], v[208:211], v[34:37]
	v_mfma_f32_16x16x32_bf16 v[26:29], v[182:185], v[216:219], v[26:29]
	v_mfma_f32_16x16x32_bf16 v[18:21], v[190:193], v[216:219], v[18:21]
	v_mfma_f32_16x16x32_bf16 v[10:13], v[182:185], v[224:227], v[10:13]
	v_mfma_f32_16x16x32_bf16 v[2:5], v[190:193], v[224:227], v[2:5]
	s_setprio 0
	s_barrier
	s_add_i32 s12, 0, 0x18000
	v_add_u32_e32 v134, s12, v152
	s_add_i32 s13, 0, 0x1c000
	ds_read_b128 v[162:165], v134
	ds_read_b128 v[166:169], v134 offset:1024
	ds_read_b128 v[170:173], v134 offset:2048
	ds_read_b128 v[174:177], v134 offset:3072
	v_add_u32_e32 v134, s13, v152
	ds_read_b128 v[178:181], v134
	ds_read_b128 v[182:185], v134 offset:1024
	ds_read_b128 v[186:189], v134 offset:2048
	ds_read_b128 v[190:193], v134 offset:3072
	s_mov_b32 m0, s79
	v_cndmask_b32_e32 v134, v138, v159, vcc
	ds_read_b128 v[194:197], v156 offset:32768
	ds_read_b128 v[198:201], v156 offset:33792
	ds_read_b128 v[204:207], v156 offset:34816
	ds_read_b128 v[208:211], v156 offset:35840
	ds_read_b128 v[212:215], v156 offset:36864
	ds_read_b128 v[216:219], v156 offset:37888
	ds_read_b128 v[220:223], v156 offset:38912
	ds_read_b128 v[224:227], v156 offset:39936
	global_load_lds_dwordx4 v134, s[10:11]
	v_cndmask_b32_e32 v134, v140, v160, vcc
	s_mov_b32 m0, s80
	s_nop 0
	global_load_lds_dwordx4 v134, s[10:11]
	s_waitcnt vmcnt(8)
	s_waitcnt lgkmcnt(0)
	s_barrier
	s_setprio 1
	v_mfma_f32_16x16x32_bf16 v[126:129], v[162:165], v[194:197], v[126:129]
	v_mfma_f32_16x16x32_bf16 v[118:121], v[170:173], v[194:197], v[118:121]
	v_mfma_f32_16x16x32_bf16 v[110:113], v[162:165], v[204:207], v[110:113]
	v_mfma_f32_16x16x32_bf16 v[102:105], v[170:173], v[204:207], v[102:105]
	v_mfma_f32_16x16x32_bf16 v[94:97], v[162:165], v[212:215], v[94:97]
	v_mfma_f32_16x16x32_bf16 v[86:89], v[170:173], v[212:215], v[86:89]
	v_mfma_f32_16x16x32_bf16 v[78:81], v[162:165], v[220:223], v[78:81]
	v_mfma_f32_16x16x32_bf16 v[70:73], v[170:173], v[220:223], v[70:73]
	v_mfma_f32_16x16x32_bf16 v[126:129], v[166:169], v[198:201], v[126:129]
	v_mfma_f32_16x16x32_bf16 v[118:121], v[174:177], v[198:201], v[118:121]
	v_mfma_f32_16x16x32_bf16 v[110:113], v[166:169], v[208:211], v[110:113]
	v_mfma_f32_16x16x32_bf16 v[102:105], v[174:177], v[208:211], v[102:105]
	v_mfma_f32_16x16x32_bf16 v[94:97], v[166:169], v[216:219], v[94:97]
	v_mfma_f32_16x16x32_bf16 v[86:89], v[174:177], v[216:219], v[86:89]
	v_mfma_f32_16x16x32_bf16 v[78:81], v[166:169], v[224:227], v[78:81]
	v_mfma_f32_16x16x32_bf16 v[70:73], v[174:177], v[224:227], v[70:73]
	v_mfma_f32_16x16x32_bf16 v[122:125], v[178:181], v[194:197], v[122:125]
	v_mfma_f32_16x16x32_bf16 v[114:117], v[186:189], v[194:197], v[114:117]
	v_mfma_f32_16x16x32_bf16 v[106:109], v[178:181], v[204:207], v[106:109]
	v_mfma_f32_16x16x32_bf16 v[98:101], v[186:189], v[204:207], v[98:101]
	v_mfma_f32_16x16x32_bf16 v[90:93], v[178:181], v[212:215], v[90:93]
	v_mfma_f32_16x16x32_bf16 v[82:85], v[186:189], v[212:215], v[82:85]
	v_mfma_f32_16x16x32_bf16 v[74:77], v[178:181], v[220:223], v[74:77]
	v_mfma_f32_16x16x32_bf16 v[66:69], v[186:189], v[220:223], v[66:69]
	v_mfma_f32_16x16x32_bf16 v[122:125], v[182:185], v[198:201], v[122:125]
	v_mfma_f32_16x16x32_bf16 v[114:117], v[190:193], v[198:201], v[114:117]
	v_mfma_f32_16x16x32_bf16 v[106:109], v[182:185], v[208:211], v[106:109]
	v_mfma_f32_16x16x32_bf16 v[98:101], v[190:193], v[208:211], v[98:101]
	v_mfma_f32_16x16x32_bf16 v[90:93], v[182:185], v[216:219], v[90:93]
	v_mfma_f32_16x16x32_bf16 v[82:85], v[190:193], v[216:219], v[82:85]
	v_mfma_f32_16x16x32_bf16 v[74:77], v[182:185], v[224:227], v[74:77]
	v_mfma_f32_16x16x32_bf16 v[66:69], v[190:193], v[224:227], v[66:69]
	s_setprio 0
	s_barrier
; #define PG8_STAGE(bufoff, gbase, voff) do { _Pragma("unroll") for (int _i = 0; _i < 2; ++_i) \
;         __builtin_amdgcn_global_load_lds((const unsigned*)((const char*)(gbase) + (voff)[_i]), (PG8_LAS unsigned*)(lds + (bufoff) + ldsw + _i * 8192), 16, 0, 0); } while (0)
; #define PG8_LDA(dst, b, h) do { _Pragma("unroll") for (int m = 0; m < 4; ++m) _Pragma("unroll") for (int k = 0; k < 2; ++k) dst[m][k] = *(const PG8_LAS bf16x8*)(lds + PG8_SA(b, h) + aoff + m * 2048 + k * 1024); } while (0)
; #define PG8_MMA(ai, bj, At, Bt) do { __builtin_amdgcn_s_setprio(1); _Pragma("unroll") for (int m = 0; m < 4; ++m) _Pragma("unroll") for (int n = 0; n < 2; ++n) _Pragma("unroll") for (int k = 0; k < 2; ++k) \
;         acc[ai][bj][m][n] = __builtin_amdgcn_mfma_f32_16x16x32_bf16(Bt[n][k], At[m][k], acc[ai][bj][m][n], 0, 0, 0); __builtin_amdgcn_s_setprio(0); } while (0)
; #define PG8_WAIT_V(n) asm volatile("s_waitcnt vmcnt(" #n ")" ::: "memory")
; #define PG8_WAIT_L(n) asm volatile("s_waitcnt lgkmcnt(" #n ")" ::: "memory")
; #define PG8_BAR __builtin_amdgcn_s_barrier()
; #define PG8_SCHED __builtin_amdgcn_sched_barrier(0)
; template <class Epi, class Sched, bool ALIGN_EPI = false, bool SP2 = false>
; __device__ __forceinline__ void gemm_phase(PG8_LAS unsigned char* lds, const Gemm g, const Sched& S, const Epi& E) {
;     ...
;             PG8_LDA(At, 1, 1); PG8_STAGE(PG8_SB(1, 0), b3, voffB); PG8_STAGE(PG8_SB(1, 1), b3 + hstep, voffB); PG8_STAGEA(PG8_SA(1, 0), a3, 0, last);
;             PG8_WAIT_V(8); PG8_WAIT_L(0); PG8_BAR; PG8_MMA(1, 0, At, B0); PG8_MMA(1, 1, At, B1); PG8_BAR; PG8_SCHED;
	s_add_i32 s10, s12, s76
	v_lshl_add_u64 v[228:229], v[228:229], 0, s[52:53]
	s_mov_b32 m0, s10
	ds_read_b128 v[194:197], v156 offset:49152
	ds_read_b128 v[198:201], v156 offset:50176
	ds_read_b128 v[204:207], v156 offset:51200
	ds_read_b128 v[208:211], v156 offset:52224
	ds_read_b128 v[212:215], v156 offset:53248
	ds_read_b128 v[216:219], v156 offset:54272
	ds_read_b128 v[220:223], v156 offset:55296
	ds_read_b128 v[224:227], v156 offset:56320
	global_load_lds_dwordx4 v[228:229], off
	s_add_i32 m0, s10, 0x2000
	s_add_u32 s8, s8, 0x80080
	v_lshl_add_u64 v[228:229], v[230:231], 0, s[52:53]
	s_addc_u32 s9, s9, 0
	s_add_i32 s10, s13, s76
	global_load_lds_dwordx4 v[228:229], off
	v_lshl_add_u64 v[228:229], s[8:9], 0, v[130:131]
	s_mov_b32 m0, s10
	s_nop 0
	global_load_lds_dwordx4 v[228:229], off
	v_lshl_add_u64 v[228:229], s[8:9], 0, v[132:133]
	s_add_i32 m0, s10, 0x2000
	s_nop 0
	global_load_lds_dwordx4 v[228:229], off
	v_lshl_add_u64 v[228:229], v[232:233], 0, s[52:53]
	s_mov_b32 m0, s81
	s_nop 0
	global_load_lds_dwordx4 v[228:229], off
	v_lshl_add_u64 v[228:229], v[234:235], 0, s[52:53]
	s_mov_b32 m0, s82
	s_nop 0
	global_load_lds_dwordx4 v[228:229], off
	s_waitcnt vmcnt(8)
	s_waitcnt lgkmcnt(0)
	s_barrier
	s_setprio 1
	v_mfma_f32_16x16x32_bf16 v[62:65], v[162:165], v[194:197], v[62:65]
	v_mfma_f32_16x16x32_bf16 v[54:57], v[170:173], v[194:197], v[54:57]
	v_mfma_f32_16x16x32_bf16 v[46:49], v[162:165], v[204:207], v[46:49]
	v_mfma_f32_16x16x32_bf16 v[38:41], v[170:173], v[204:207], v[38:41]
	v_mfma_f32_16x16x32_bf16 v[30:33], v[162:165], v[212:215], v[30:33]
	v_mfma_f32_16x16x32_bf16 v[22:25], v[170:173], v[212:215], v[22:25]
	v_mfma_f32_16x16x32_bf16 v[14:17], v[162:165], v[220:223], v[14:17]
	v_mfma_f32_16x16x32_bf16 v[6:9], v[170:173], v[220:223], v[6:9]
	v_mfma_f32_16x16x32_bf16 v[62:65], v[166:169], v[198:201], v[62:65]
	v_mfma_f32_16x16x32_bf16 v[54:57], v[174:177], v[198:201], v[54:57]
	v_mfma_f32_16x16x32_bf16 v[46:49], v[166:169], v[208:211], v[46:49]
	v_mfma_f32_16x16x32_bf16 v[38:41], v[174:177], v[208:211], v[38:41]
	v_mfma_f32_16x16x32_bf16 v[30:33], v[166:169], v[216:219], v[30:33]
	v_mfma_f32_16x16x32_bf16 v[22:25], v[174:177], v[216:219], v[22:25]
	v_mfma_f32_16x16x32_bf16 v[14:17], v[166:169], v[224:227], v[14:17]
	v_mfma_f32_16x16x32_bf16 v[6:9], v[174:177], v[224:227], v[6:9]
	v_mfma_f32_16x16x32_bf16 v[58:61], v[178:181], v[194:197], v[58:61]
	v_mfma_f32_16x16x32_bf16 v[50:53], v[186:189], v[194:197], v[50:53]
	v_mfma_f32_16x16x32_bf16 v[42:45], v[178:181], v[204:207], v[42:45]
	v_mfma_f32_16x16x32_bf16 v[34:37], v[186:189], v[204:207], v[34:37]
	v_mfma_f32_16x16x32_bf16 v[26:29], v[178:181], v[212:215], v[26:29]
	v_mfma_f32_16x16x32_bf16 v[18:21], v[186:189], v[212:215], v[18:21]
	v_mfma_f32_16x16x32_bf16 v[10:13], v[178:181], v[220:223], v[10:13]
	v_mfma_f32_16x16x32_bf16 v[2:5], v[186:189], v[220:223], v[2:5]
	v_mfma_f32_16x16x32_bf16 v[58:61], v[182:185], v[198:201], v[58:61]
	v_mfma_f32_16x16x32_bf16 v[50:53], v[190:193], v[198:201], v[50:53]
	v_mfma_f32_16x16x32_bf16 v[42:45], v[182:185], v[208:211], v[42:45]
	v_mfma_f32_16x16x32_bf16 v[34:37], v[190:193], v[208:211], v[34:37]
	v_mfma_f32_16x16x32_bf16 v[26:29], v[182:185], v[216:219], v[26:29]
	v_mfma_f32_16x16x32_bf16 v[18:21], v[190:193], v[216:219], v[18:21]
	v_mfma_f32_16x16x32_bf16 v[10:13], v[182:185], v[224:227], v[10:13]
	v_mfma_f32_16x16x32_bf16 v[2:5], v[190:193], v[224:227], v[2:5]
	s_setprio 0
	s_barrier
	s_add_i32 s19, s19, 2
	s_cmp_gt_u32 s19, 29
	s_mov_b64 s[12:13], s[6:7]
	s_cbranch_scc0 .LBB0_792
	s_and_b64 vcc, exec, s[56:57]
	s_cbranch_vccz .LBB0_795
	s_barrier

; #define PG8_STAGE(bufoff, gbase, voff) do { _Pragma("unroll") for (int _i = 0; _i < 2; ++_i) \
;         __builtin_amdgcn_global_load_lds((const unsigned*)((const char*)(gbase) + (voff)[_i]), (PG8_LAS unsigned*)(lds + (bufoff) + ldsw + _i * 8192), 16, 0, 0); } while (0)
; #define PG8_LDA(dst, b, h) do { _Pragma("unroll") for (int m = 0; m < 4; ++m) _Pragma("unroll") for (int k = 0; k < 2; ++k) dst[m][k] = *(const PG8_LAS bf16x8*)(lds + PG8_SA(b, h) + aoff + m * 2048 + k * 1024); } while (0)
; #define PG8_LDB(dst, b, h) do { _Pragma("unroll") for (int n = 0; n < 2; ++n) _Pragma("unroll") for (int k = 0; k < 2; ++k) dst[n][k] = *(const PG8_LAS bf16x8*)(lds + PG8_SB(b, h) + boff + n * 2048 + k * 1024); } while (0)
; #define PG8_MMA(ai, bj, At, Bt) do { __builtin_amdgcn_s_setprio(1); _Pragma("unroll") for (int m = 0; m < 4; ++m) _Pragma("unroll") for (int n = 0; n < 2; ++n) _Pragma("unroll") for (int k = 0; k < 2; ++k) \
;         acc[ai][bj][m][n] = __builtin_amdgcn_mfma_f32_16x16x32_bf16(Bt[n][k], At[m][k], acc[ai][bj][m][n], 0, 0, 0); __builtin_amdgcn_s_setprio(0); } while (0)
; #define PG8_WAIT_V(n) asm volatile("s_waitcnt vmcnt(" #n ")" ::: "memory")
; #define PG8_WAIT_L(n) asm volatile("s_waitcnt lgkmcnt(" #n ")" ::: "memory")
; template <class Epi, class Sched, bool ALIGN_EPI = false, bool SP2 = false>
; __device__ __forceinline__ void gemm_phase(PG8_LAS unsigned char* lds, const Gemm g, const Sched& S, const Epi& E) {
;     ...
;             const bool last = (t == nt - 2);
;             const char* a1 = cA + (size_t)(t + 1) * kstep;
;             const char* a2 = last ? nA : cA + (size_t)(t + 2) * kstep; const char* b2 = last ? nB : cB + (size_t)(t + 2) * kstep;
;             const char* a3 = a2 + kstep; const char* b3 = b2 + kstep;
;             if (last && has_next) S.a_ready(nxt);
;             if constexpr (SP2) {
;             PG8_LDB(B0, 0, 0); PG8_LDB(B1, 0, 1); PG8_SCHED; PG8_LDA(At, 0, 0); PG8_STAGEA(PG8_SA(1, 1), a1, 1, false);
;             PG8_WAIT_V(8); PG8_WAIT_L(0); PG8_BAR; PG8_MMA(0, 0, At, B0); PG8_MMA(0, 1, At, B1); PG8_BAR; PG8_SCHED;
;             PG8_LDA(At, 0, 1); PG8_STAGE(PG8_SB(0, 0), b2, voffB); PG8_STAGE(PG8_SB(0, 1), b2 + hstep, voffB); PG8_STAGEA(PG8_SA(0, 0), a2, 0, last);
;             PG8_WAIT_V(8); PG8_WAIT_L(0); PG8_BAR; PG8_MMA(1, 0, At, B0); PG8_MMA(1, 1, At, B1); PG8_BAR; PG8_SCHED;
.LBB0_927:
	v_add_u32_e32 v147, s76, v142
	ds_read_b128 v[148:151], v147
	ds_read_b128 v[152:155], v147 offset:1024
	ds_read_b128 v[156:159], v147 offset:2048
	ds_read_b128 v[160:163], v147 offset:3072
	v_add_u32_e32 v147, s77, v142
	ds_read_b128 v[164:167], v147
	ds_read_b128 v[168:171], v147 offset:1024
	ds_read_b128 v[172:175], v147 offset:2048
	ds_read_b128 v[176:179], v147 offset:3072
	s_add_u32 s60, s58, 0xfffe0080
	s_addc_u32 s61, s59, -1
	s_cmp_eq_u32 s83, 4
	s_cselect_b32 s63, s9, s61
	s_cselect_b32 s62, s11, s60
	s_cselect_b32 s61, s36, s49
	s_cselect_b32 s60, s37, s47
	v_lshl_add_u64 v[200:201], s[58:59], 0, v[138:139]
	s_add_i32 m0, s57, 0xc000
	ds_read_b128 v[180:183], v146
	ds_read_b128 v[184:187], v146 offset:1024
	ds_read_b128 v[188:191], v146 offset:2048
	ds_read_b128 v[192:195], v146 offset:3072
	ds_read_b128 v[196:199], v146 offset:4096
	ds_read_b128 v[204:207], v146 offset:5120
	ds_read_b128 v[208:211], v146 offset:6144
	ds_read_b128 v[212:215], v146 offset:7168
	global_load_lds_dwordx4 v[200:201], off
	v_lshl_add_u64 v[200:201], s[58:59], 0, v[140:141]
	s_add_i32 m0, s57, 0xe000
	s_nop 0
	global_load_lds_dwordx4 v[200:201], off
	s_waitcnt vmcnt(8)
	s_waitcnt lgkmcnt(0)
	s_barrier
	s_setprio 1
	v_mfma_f32_16x16x32_bf16 v[122:125], v[148:151], v[180:183], v[122:125]
	v_mfma_f32_16x16x32_bf16 v[126:129], v[156:159], v[180:183], v[126:129]
	v_mfma_f32_16x16x32_bf16 v[106:109], v[148:151], v[188:191], v[106:109]
	v_mfma_f32_16x16x32_bf16 v[110:113], v[156:159], v[188:191], v[110:113]
	v_mfma_f32_16x16x32_bf16 v[90:93], v[148:151], v[196:199], v[90:93]
	v_mfma_f32_16x16x32_bf16 v[94:97], v[156:159], v[196:199], v[94:97]
	v_mfma_f32_16x16x32_bf16 v[74:77], v[148:151], v[208:211], v[74:77]
	v_mfma_f32_16x16x32_bf16 v[78:81], v[156:159], v[208:211], v[78:81]
	v_mfma_f32_16x16x32_bf16 v[122:125], v[152:155], v[184:187], v[122:125]
	v_mfma_f32_16x16x32_bf16 v[126:129], v[160:163], v[184:187], v[126:129]
	v_mfma_f32_16x16x32_bf16 v[106:109], v[152:155], v[192:195], v[106:109]
	v_mfma_f32_16x16x32_bf16 v[110:113], v[160:163], v[192:195], v[110:113]
	v_mfma_f32_16x16x32_bf16 v[90:93], v[152:155], v[204:207], v[90:93]
	v_mfma_f32_16x16x32_bf16 v[94:97], v[160:163], v[204:207], v[94:97]
	v_mfma_f32_16x16x32_bf16 v[74:77], v[152:155], v[212:215], v[74:77]
	v_mfma_f32_16x16x32_bf16 v[78:81], v[160:163], v[212:215], v[78:81]
	v_mfma_f32_16x16x32_bf16 v[114:117], v[164:167], v[180:183], v[114:117]
	v_mfma_f32_16x16x32_bf16 v[118:121], v[172:175], v[180:183], v[118:121]
	v_mfma_f32_16x16x32_bf16 v[98:101], v[164:167], v[188:191], v[98:101]
	v_mfma_f32_16x16x32_bf16 v[102:105], v[172:175], v[188:191], v[102:105]
	v_mfma_f32_16x16x32_bf16 v[82:85], v[164:167], v[196:199], v[82:85]
	v_mfma_f32_16x16x32_bf16 v[86:89], v[172:175], v[196:199], v[86:89]
	v_mfma_f32_16x16x32_bf16 v[66:69], v[164:167], v[208:211], v[66:69]
	v_mfma_f32_16x16x32_bf16 v[70:73], v[172:175], v[208:211], v[70:73]
	v_mfma_f32_16x16x32_bf16 v[114:117], v[168:171], v[184:187], v[114:117]
	v_mfma_f32_16x16x32_bf16 v[118:121], v[176:179], v[184:187], v[118:121]
	v_mfma_f32_16x16x32_bf16 v[98:101], v[168:171], v[192:195], v[98:101]
	v_mfma_f32_16x16x32_bf16 v[102:105], v[176:179], v[192:195], v[102:105]
	v_mfma_f32_16x16x32_bf16 v[82:85], v[168:171], v[204:207], v[82:85]
	v_mfma_f32_16x16x32_bf16 v[86:89], v[176:179], v[204:207], v[86:89]
	v_mfma_f32_16x16x32_bf16 v[66:69], v[168:171], v[212:215], v[66:69]
	v_mfma_f32_16x16x32_bf16 v[70:73], v[176:179], v[212:215], v[70:73]
	s_setprio 0
	s_barrier
	s_add_i32 s84, s76, s65
	v_lshl_add_u64 v[200:201], s[60:61], 0, v[132:133]
	s_mov_b32 m0, s84
	ds_read_b128 v[180:183], v146 offset:16384
	ds_read_b128 v[184:187], v146 offset:17408
	ds_read_b128 v[188:191], v146 offset:18432
	ds_read_b128 v[192:195], v146 offset:19456
	ds_read_b128 v[196:199], v146 offset:20480
	ds_read_b128 v[204:207], v146 offset:21504
	ds_read_b128 v[208:211], v146 offset:22528
	ds_read_b128 v[212:215], v146 offset:23552
	global_load_lds_dwordx4 v[200:201], off
	s_add_i32 m0, s84, 0x2000
	s_add_u32 s84, s60, 0x20000
	v_lshl_add_u64 v[216:217], s[60:61], 0, v[136:137]
	s_addc_u32 s85, s61, 0
	s_add_i32 s86, s77, s65
	global_load_lds_dwordx4 v[216:217], off
	v_lshl_add_u64 v[218:219], s[84:85], 0, v[132:133]
	s_mov_b32 m0, s86
	v_lshl_add_u64 v[220:221], s[62:63], 0, v[134:135]
	global_load_lds_dwordx4 v[218:219], off
	v_lshl_add_u64 v[218:219], s[84:85], 0, v[136:137]
	s_add_i32 m0, s86, 0x2000
	s_nop 0
	global_load_lds_dwordx4 v[218:219], off
	v_lshl_add_u64 v[218:219], s[62:63], 0, v[130:131]
	s_mov_b32 m0, s57
	s_nop 0
	global_load_lds_dwordx4 v[218:219], off
	s_mov_b32 m0, s66
	s_nop 0
	global_load_lds_dwordx4 v[220:221], off
	s_waitcnt vmcnt(8)
	s_waitcnt lgkmcnt(0)
	s_barrier
; #define PG8_LDA(dst, b, h) do { _Pragma("unroll") for (int m = 0; m < 4; ++m) _Pragma("unroll") for (int k = 0; k < 2; ++k) dst[m][k] = *(const PG8_LAS bf16x8*)(lds + PG8_SA(b, h) + aoff + m * 2048 + k * 1024); } while (0)
; #define PG8_LDB(dst, b, h) do { _Pragma("unroll") for (int n = 0; n < 2; ++n) _Pragma("unroll") for (int k = 0; k < 2; ++k) dst[n][k] = *(const PG8_LAS bf16x8*)(lds + PG8_SB(b, h) + boff + n * 2048 + k * 1024); } while (0)
; #define PG8_MMA(ai, bj, At, Bt) do { __builtin_amdgcn_s_setprio(1); _Pragma("unroll") for (int m = 0; m < 4; ++m) _Pragma("unroll") for (int n = 0; n < 2; ++n) _Pragma("unroll") for (int k = 0; k < 2; ++k) \
;         acc[ai][bj][m][n] = __builtin_amdgcn_mfma_f32_16x16x32_bf16(Bt[n][k], At[m][k], acc[ai][bj][m][n], 0, 0, 0); __builtin_amdgcn_s_setprio(0); } while (0)
; #define PG8_WAIT_V(n) asm volatile("s_waitcnt vmcnt(" #n ")" ::: "memory")
; #define PG8_WAIT_L(n) asm volatile("s_waitcnt lgkmcnt(" #n ")" ::: "memory")
; #define PG8_BAR __builtin_amdgcn_s_barrier()
; #define PG8_SCHED __builtin_amdgcn_sched_barrier(0)
; template <class Epi, class Sched, bool ALIGN_EPI = false, bool SP2 = false>
; __device__ __forceinline__ void gemm_phase(PG8_LAS unsigned char* lds, const Gemm g, const Sched& S, const Epi& E) {
;     ...
;             PG8_WAIT_V(8); PG8_WAIT_L(0); PG8_BAR; PG8_MMA(1, 0, At, B0); PG8_MMA(1, 1, At, B1); PG8_BAR; PG8_SCHED;
;             PG8_LDB(B0, 1, 0); PG8_LDB(B1, 1, 1); PG8_SCHED; PG8_LDA(At, 1, 0); PG8_STAGEA(PG8_SA(0, 1), a2, 1, last);
;             PG8_WAIT_V(8); PG8_WAIT_L(0); PG8_BAR; PG8_MMA(0, 0, At, B0); PG8_MMA(0, 1, At, B1); PG8_BAR; PG8_SCHED;
	s_setprio 1
	v_mfma_f32_16x16x32_bf16 v[58:61], v[148:151], v[180:183], v[58:61]
	v_mfma_f32_16x16x32_bf16 v[62:65], v[156:159], v[180:183], v[62:65]
	v_mfma_f32_16x16x32_bf16 v[42:45], v[148:151], v[188:191], v[42:45]
	v_mfma_f32_16x16x32_bf16 v[46:49], v[156:159], v[188:191], v[46:49]
	v_mfma_f32_16x16x32_bf16 v[26:29], v[148:151], v[196:199], v[26:29]
	v_mfma_f32_16x16x32_bf16 v[30:33], v[156:159], v[196:199], v[30:33]
	v_mfma_f32_16x16x32_bf16 v[10:13], v[148:151], v[208:211], v[10:13]
	v_mfma_f32_16x16x32_bf16 v[14:17], v[156:159], v[208:211], v[14:17]
	v_mfma_f32_16x16x32_bf16 v[58:61], v[152:155], v[184:187], v[58:61]
	v_mfma_f32_16x16x32_bf16 v[62:65], v[160:163], v[184:187], v[62:65]
	v_mfma_f32_16x16x32_bf16 v[42:45], v[152:155], v[192:195], v[42:45]
	v_mfma_f32_16x16x32_bf16 v[46:49], v[160:163], v[192:195], v[46:49]
	v_mfma_f32_16x16x32_bf16 v[26:29], v[152:155], v[204:207], v[26:29]
	v_mfma_f32_16x16x32_bf16 v[30:33], v[160:163], v[204:207], v[30:33]
	v_mfma_f32_16x16x32_bf16 v[10:13], v[152:155], v[212:215], v[10:13]
	v_mfma_f32_16x16x32_bf16 v[14:17], v[160:163], v[212:215], v[14:17]
	v_mfma_f32_16x16x32_bf16 v[50:53], v[164:167], v[180:183], v[50:53]
	v_mfma_f32_16x16x32_bf16 v[54:57], v[172:175], v[180:183], v[54:57]
	v_mfma_f32_16x16x32_bf16 v[34:37], v[164:167], v[188:191], v[34:37]
	v_mfma_f32_16x16x32_bf16 v[38:41], v[172:175], v[188:191], v[38:41]
	v_mfma_f32_16x16x32_bf16 v[18:21], v[164:167], v[196:199], v[18:21]
	v_mfma_f32_16x16x32_bf16 v[22:25], v[172:175], v[196:199], v[22:25]
	v_mfma_f32_16x16x32_bf16 v[6:9], v[164:167], v[208:211], v[6:9]
	v_mfma_f32_16x16x32_bf16 v[2:5], v[172:175], v[208:211], v[2:5]
	v_mfma_f32_16x16x32_bf16 v[50:53], v[168:171], v[184:187], v[50:53]
	v_mfma_f32_16x16x32_bf16 v[54:57], v[176:179], v[184:187], v[54:57]
	v_mfma_f32_16x16x32_bf16 v[34:37], v[168:171], v[192:195], v[34:37]
	v_mfma_f32_16x16x32_bf16 v[38:41], v[176:179], v[192:195], v[38:41]
	v_mfma_f32_16x16x32_bf16 v[18:21], v[168:171], v[204:207], v[18:21]
	v_mfma_f32_16x16x32_bf16 v[22:25], v[176:179], v[204:207], v[22:25]
	v_mfma_f32_16x16x32_bf16 v[6:9], v[168:171], v[212:215], v[6:9]
	v_mfma_f32_16x16x32_bf16 v[2:5], v[176:179], v[212:215], v[2:5]
	s_setprio 0
	s_barrier
	s_add_i32 s84, 0, 0x18000
	v_add_u32_e32 v147, s84, v142
	s_add_i32 s85, 0, 0x1c000
	ds_read_b128 v[148:151], v147
	ds_read_b128 v[152:155], v147 offset:1024
	ds_read_b128 v[156:159], v147 offset:2048
	ds_read_b128 v[160:163], v147 offset:3072
	v_add_u32_e32 v147, s85, v142
	ds_read_b128 v[164:167], v147
	ds_read_b128 v[168:171], v147 offset:1024
	ds_read_b128 v[172:175], v147 offset:2048
	ds_read_b128 v[176:179], v147 offset:3072
	s_add_u32 s62, s62, 0x20000
	s_addc_u32 s63, s63, 0
	s_mov_b32 m0, s67
	v_lshl_add_u64 v[222:223], s[62:63], 0, v[130:131]
	ds_read_b128 v[180:183], v146 offset:32768
	ds_read_b128 v[184:187], v146 offset:33792
	ds_read_b128 v[188:191], v146 offset:34816
	ds_read_b128 v[192:195], v146 offset:35840
	ds_read_b128 v[196:199], v146 offset:36864
	ds_read_b128 v[204:207], v146 offset:37888
	ds_read_b128 v[208:211], v146 offset:38912
	ds_read_b128 v[212:215], v146 offset:39936
	global_load_lds_dwordx4 v[222:223], off
	v_lshl_add_u64 v[222:223], s[62:63], 0, v[134:135]
	s_mov_b32 m0, s68
	s_nop 0
	global_load_lds_dwordx4 v[222:223], off
	s_waitcnt vmcnt(8)
	s_waitcnt lgkmcnt(0)
	s_barrier
	s_setprio 1
	v_mfma_f32_16x16x32_bf16 v[122:125], v[148:151], v[180:183], v[122:125]
	v_mfma_f32_16x16x32_bf16 v[126:129], v[156:159], v[180:183], v[126:129]
	v_mfma_f32_16x16x32_bf16 v[106:109], v[148:151], v[188:191], v[106:109]
	v_mfma_f32_16x16x32_bf16 v[110:113], v[156:159], v[188:191], v[110:113]
	v_mfma_f32_16x16x32_bf16 v[90:93], v[148:151], v[196:199], v[90:93]
	v_mfma_f32_16x16x32_bf16 v[94:97], v[156:159], v[196:199], v[94:97]
	v_mfma_f32_16x16x32_bf16 v[74:77], v[148:151], v[208:211], v[74:77]
	v_mfma_f32_16x16x32_bf16 v[78:81], v[156:159], v[208:211], v[78:81]
	v_mfma_f32_16x16x32_bf16 v[122:125], v[152:155], v[184:187], v[122:125]
	v_mfma_f32_16x16x32_bf16 v[126:129], v[160:163], v[184:187], v[126:129]
	v_mfma_f32_16x16x32_bf16 v[106:109], v[152:155], v[192:195], v[106:109]
	v_mfma_f32_16x16x32_bf16 v[110:113], v[160:163], v[192:195], v[110:113]
	v_mfma_f32_16x16x32_bf16 v[90:93], v[152:155], v[204:207], v[90:93]
	v_mfma_f32_16x16x32_bf16 v[94:97], v[160:163], v[204:207], v[94:97]
	v_mfma_f32_16x16x32_bf16 v[74:77], v[152:155], v[212:215], v[74:77]
	v_mfma_f32_16x16x32_bf16 v[78:81], v[160:163], v[212:215], v[78:81]
	v_mfma_f32_16x16x32_bf16 v[114:117], v[164:167], v[180:183], v[114:117]
	v_mfma_f32_16x16x32_bf16 v[118:121], v[172:175], v[180:183], v[118:121]
	v_mfma_f32_16x16x32_bf16 v[98:101], v[164:167], v[188:191], v[98:101]
	v_mfma_f32_16x16x32_bf16 v[102:105], v[172:175], v[188:191], v[102:105]
	v_mfma_f32_16x16x32_bf16 v[82:85], v[164:167], v[196:199], v[82:85]
	v_mfma_f32_16x16x32_bf16 v[86:89], v[172:175], v[196:199], v[86:89]
	v_mfma_f32_16x16x32_bf16 v[66:69], v[164:167], v[208:211], v[66:69]
	v_mfma_f32_16x16x32_bf16 v[70:73], v[172:175], v[208:211], v[70:73]
	v_mfma_f32_16x16x32_bf16 v[114:117], v[168:171], v[184:187], v[114:117]
	v_mfma_f32_16x16x32_bf16 v[118:121], v[176:179], v[184:187], v[118:121]
	v_mfma_f32_16x16x32_bf16 v[98:101], v[168:171], v[192:195], v[98:101]
	v_mfma_f32_16x16x32_bf16 v[102:105], v[176:179], v[192:195], v[102:105]
	v_mfma_f32_16x16x32_bf16 v[82:85], v[168:171], v[204:207], v[82:85]
	v_mfma_f32_16x16x32_bf16 v[86:89], v[176:179], v[204:207], v[86:89]
	v_mfma_f32_16x16x32_bf16 v[66:69], v[168:171], v[212:215], v[66:69]
	v_mfma_f32_16x16x32_bf16 v[70:73], v[176:179], v[212:215], v[70:73]
	s_setprio 0
	s_barrier
; #define PG8_STAGE(bufoff, gbase, voff) do { _Pragma("unroll") for (int _i = 0; _i < 2; ++_i) \
;         __builtin_amdgcn_global_load_lds((const unsigned*)((const char*)(gbase) + (voff)[_i]), (PG8_LAS unsigned*)(lds + (bufoff) + ldsw + _i * 8192), 16, 0, 0); } while (0)
; #define PG8_LDA(dst, b, h) do { _Pragma("unroll") for (int m = 0; m < 4; ++m) _Pragma("unroll") for (int k = 0; k < 2; ++k) dst[m][k] = *(const PG8_LAS bf16x8*)(lds + PG8_SA(b, h) + aoff + m * 2048 + k * 1024); } while (0)
; #define PG8_MMA(ai, bj, At, Bt) do { __builtin_amdgcn_s_setprio(1); _Pragma("unroll") for (int m = 0; m < 4; ++m) _Pragma("unroll") for (int n = 0; n < 2; ++n) _Pragma("unroll") for (int k = 0; k < 2; ++k) \
;         acc[ai][bj][m][n] = __builtin_amdgcn_mfma_f32_16x16x32_bf16(Bt[n][k], At[m][k], acc[ai][bj][m][n], 0, 0, 0); __builtin_amdgcn_s_setprio(0); } while (0)
; #define PG8_WAIT_V(n) asm volatile("s_waitcnt vmcnt(" #n ")" ::: "memory")
; #define PG8_WAIT_L(n) asm volatile("s_waitcnt lgkmcnt(" #n ")" ::: "memory")
; #define PG8_BAR __builtin_amdgcn_s_barrier()
; #define PG8_SCHED __builtin_amdgcn_sched_barrier(0)
; template <class Epi, class Sched, bool ALIGN_EPI = false, bool SP2 = false>
; __device__ __forceinline__ void gemm_phase(PG8_LAS unsigned char* lds, const Gemm g, const Sched& S, const Epi& E) {
;     ...
;             PG8_LDA(At, 1, 1); PG8_STAGE(PG8_SB(1, 0), b3, voffB); PG8_STAGE(PG8_SB(1, 1), b3 + hstep, voffB); PG8_STAGEA(PG8_SA(1, 0), a3, 0, last);
;             PG8_WAIT_V(8); PG8_WAIT_L(0); PG8_BAR; PG8_MMA(1, 0, At, B0); PG8_MMA(1, 1, At, B1); PG8_BAR; PG8_SCHED;
	s_add_i32 s62, s84, s65
	v_lshl_add_u64 v[200:201], v[200:201], 0, s[18:19]
	s_mov_b32 m0, s62
	ds_read_b128 v[180:183], v146 offset:49152
	ds_read_b128 v[184:187], v146 offset:50176
	ds_read_b128 v[188:191], v146 offset:51200
	ds_read_b128 v[192:195], v146 offset:52224
	ds_read_b128 v[196:199], v146 offset:53248
	ds_read_b128 v[204:207], v146 offset:54272
	ds_read_b128 v[208:211], v146 offset:55296
	ds_read_b128 v[212:215], v146 offset:56320
	global_load_lds_dwordx4 v[200:201], off
	s_add_i32 m0, s62, 0x2000
	s_add_u32 s60, s60, 0x20080
	v_lshl_add_u64 v[200:201], v[216:217], 0, s[18:19]
	s_addc_u32 s61, s61, 0
	s_add_i32 s62, s85, s65
	global_load_lds_dwordx4 v[200:201], off
	v_lshl_add_u64 v[200:201], s[60:61], 0, v[132:133]
	s_mov_b32 m0, s62
	s_nop 0
	global_load_lds_dwordx4 v[200:201], off
	v_lshl_add_u64 v[200:201], s[60:61], 0, v[136:137]
	s_add_i32 m0, s62, 0x2000
	s_nop 0
	global_load_lds_dwordx4 v[200:201], off
	v_lshl_add_u64 v[200:201], v[218:219], 0, s[18:19]
	s_mov_b32 m0, s69
	s_nop 0
	global_load_lds_dwordx4 v[200:201], off
	v_lshl_add_u64 v[200:201], v[220:221], 0, s[18:19]
	s_mov_b32 m0, s74
	s_nop 0
	global_load_lds_dwordx4 v[200:201], off
	s_waitcnt vmcnt(8)
	s_waitcnt lgkmcnt(0)
	s_barrier
	s_setprio 1
	v_mfma_f32_16x16x32_bf16 v[58:61], v[148:151], v[180:183], v[58:61]
	v_mfma_f32_16x16x32_bf16 v[62:65], v[156:159], v[180:183], v[62:65]
	v_mfma_f32_16x16x32_bf16 v[42:45], v[148:151], v[188:191], v[42:45]
	v_mfma_f32_16x16x32_bf16 v[46:49], v[156:159], v[188:191], v[46:49]
	v_mfma_f32_16x16x32_bf16 v[26:29], v[148:151], v[196:199], v[26:29]
	v_mfma_f32_16x16x32_bf16 v[30:33], v[156:159], v[196:199], v[30:33]
	v_mfma_f32_16x16x32_bf16 v[10:13], v[148:151], v[208:211], v[10:13]
	v_mfma_f32_16x16x32_bf16 v[14:17], v[156:159], v[208:211], v[14:17]
	v_mfma_f32_16x16x32_bf16 v[58:61], v[152:155], v[184:187], v[58:61]
	v_mfma_f32_16x16x32_bf16 v[62:65], v[160:163], v[184:187], v[62:65]
	v_mfma_f32_16x16x32_bf16 v[42:45], v[152:155], v[192:195], v[42:45]
	v_mfma_f32_16x16x32_bf16 v[46:49], v[160:163], v[192:195], v[46:49]
	v_mfma_f32_16x16x32_bf16 v[26:29], v[152:155], v[204:207], v[26:29]
	v_mfma_f32_16x16x32_bf16 v[30:33], v[160:163], v[204:207], v[30:33]
	v_mfma_f32_16x16x32_bf16 v[10:13], v[152:155], v[212:215], v[10:13]
	v_mfma_f32_16x16x32_bf16 v[14:17], v[160:163], v[212:215], v[14:17]
	v_mfma_f32_16x16x32_bf16 v[50:53], v[164:167], v[180:183], v[50:53]
	v_mfma_f32_16x16x32_bf16 v[54:57], v[172:175], v[180:183], v[54:57]
	v_mfma_f32_16x16x32_bf16 v[34:37], v[164:167], v[188:191], v[34:37]
	v_mfma_f32_16x16x32_bf16 v[38:41], v[172:175], v[188:191], v[38:41]
	v_mfma_f32_16x16x32_bf16 v[18:21], v[164:167], v[196:199], v[18:21]
	v_mfma_f32_16x16x32_bf16 v[22:25], v[172:175], v[196:199], v[22:25]
	v_mfma_f32_16x16x32_bf16 v[6:9], v[164:167], v[208:211], v[6:9]
	v_mfma_f32_16x16x32_bf16 v[2:5], v[172:175], v[208:211], v[2:5]
	v_mfma_f32_16x16x32_bf16 v[50:53], v[168:171], v[184:187], v[50:53]
	v_mfma_f32_16x16x32_bf16 v[54:57], v[176:179], v[184:187], v[54:57]
	v_mfma_f32_16x16x32_bf16 v[34:37], v[168:171], v[192:195], v[34:37]
	v_mfma_f32_16x16x32_bf16 v[38:41], v[176:179], v[192:195], v[38:41]
	v_mfma_f32_16x16x32_bf16 v[18:21], v[168:171], v[204:207], v[18:21]
	v_mfma_f32_16x16x32_bf16 v[22:25], v[176:179], v[204:207], v[22:25]
	v_mfma_f32_16x16x32_bf16 v[6:9], v[168:171], v[212:215], v[6:9]
	v_mfma_f32_16x16x32_bf16 v[2:5], v[176:179], v[212:215], v[2:5]
	s_setprio 0
	s_barrier
	s_add_i32 s83, s83, 2
	s_add_u32 s58, s58, 0x100
	s_addc_u32 s59, s59, 0
	s_add_u32 s47, s47, 0x100
	s_addc_u32 s49, s49, 0
	s_cmp_gt_u32 s83, 5
	s_cbranch_scc0 .LBB0_927
	s_and_b64 vcc, exec, s[24:25]
	s_cbranch_vccz .LBB0_930
	s_barrier
